# v045 + GEMM first-unit prologue: second staging group issued before the first wait (14 DMA pieces in flight, vmcnt(2)->vmcnt(8))
# baseline (speedup 1.0000x reference)
; __device__ __forceinline__ int tidx() { int t = threadIdx.x; asm volatile("" : "+v"(t)); return t; }
; __host__ __device__ __forceinline__ int lds_byte(int r, int c) { return (r >> 3) * 1024 + (r & 7) * 128 + ((((c >> 3) ^ r) & 7) << 4) + (c & 7) * 2; }
; #define PG8_STAGE(bufoff, gbase, voff) do { _Pragma("unroll") for (int _i = 0; _i < 2; ++_i) \
;         __builtin_amdgcn_global_load_lds((const unsigned*)((const char*)(gbase) + (voff)[_i]), (LAS unsigned*)(lds + (bufoff) + ldsw + _i * 8192), 16, 0, 0); } while (0)
; #define PG8_WAIT_V(n) asm volatile("s_waitcnt vmcnt(" #n ")" ::: "memory")
; #define PG8_BAR __builtin_amdgcn_s_barrier()
;     const int tid = tidx(), wid = __builtin_amdgcn_readfirstlane(tid >> 6), lane = tid & 63, wr = wid >> 2, wc = wid & 3, fr = lane & 15, fq = lane >> 4;
;     const int K = (int)g.K, ntf = K / BK;
;     int sR[2], sC[2]; unsigned voffB[2], voffA[2][2], voffN[2][2];
; #pragma unroll
;     for (int i = 0; i < 2; ++i) { stage_rc(tid * 16 + i * 8192, sR[i], sC[i]); const int Rb = Epi::PERM ? ((sR[i] & ~31) + perm32(sR[i] & 31)) : sR[i];
;         voffB[i] = (TILED & 2) ? (unsigned)(Rb * BK + sC[i]) * 2u : (unsigned)(Rb * K + sC[i]) * 2u; }
;     constexpr size_t kstepA = (TILED & 1) ? (size_t)HALF * BK * 2 : (size_t)(BK * 2), kstepB = (TILED & 2) ? (size_t)HALF * BK * 2 : (size_t)(BK * 2);
;     const size_t hstep = (size_t)HALF * K * 2;
;     const size_t tstep = 2 * hstep;
;     const unsigned ldsw = (unsigned)wid * 1024u;
;     const int aoff = lds_byte(wr * 64 + fr, fq * 8), boff = lds_byte(wc * 32 + fr, fq * 8);
;     ...
;     const char* cA = (const char*)(g.A + (size_t)cur.z * g.aStrideZ) + (GATHER ? (size_t)0 : (size_t)cur.pm * tstep) + k0t(cur) * kstepA;
;     const char* cB = (const char*)(g.Bt + (size_t)cur.z * g.bStrideZ) + (size_t)cur.pn * tstep + k0t(cur) * kstepB;
;     PG8_STAGE(PG8_SB(0, 0), cB, voffB); PG8_STAGE(PG8_SB(0, 1), cB + hstep, voffB); PG8_STAGE(PG8_SA(0, 0), cA, voffA[0]); PG8_STAGE(PG8_SA(0, 1), cA, voffA[1]);
;     if (wr == 1) PG8_BAR;
;     PG8_WAIT_V(2); PG8_BAR;
;     PG8_STAGE(PG8_SB(1, 0), cB + kstepB, voffB); PG8_STAGE(PG8_SA(1, 0), cA + kstepA, voffA[0]); PG8_STAGE(PG8_SB(1, 1), cB + hstep + kstepB, voffB);
;     PG8_WAIT_V(6); PG8_BAR;
.LBB0_182:
	s_lshl_b32 s14, s1, 5
	s_lshl_b32 s49, s0, 6
	s_and_b32 s50, s14, 0x60
	s_add_u32 s0, s4, 0x4000
	s_addc_u32 s1, s5, 0
	s_add_i32 m0, s25, 0x18000
	v_lshl_add_u64 v[14:15], s[0:1], 0, v[130:131]
	global_load_lds_dwordx4 v[14:15], off
	v_lshl_add_u64 v[14:15], s[0:1], 0, v[132:133]
	s_add_i32 m0, s25, 0x1a000
	s_mov_b64 s[8:9], 0x80
	s_add_i32 s51, s25, 0x8000
	s_add_i32 s54, s25, 0xa000
	global_load_lds_dwordx4 v[14:15], off
	v_lshl_add_u64 v[2:3], v[2:3], 0, s[8:9]
	s_mov_b32 m0, s51
	s_add_u32 s0, s4, 0x44000
	global_load_lds_dwordx4 v[2:3], off
	v_lshl_add_u64 v[2:3], v[4:5], 0, s[8:9]
	s_mov_b32 m0, s54
	s_addc_u32 s1, s5, 0
	global_load_lds_dwordx4 v[2:3], off
	s_add_i32 m0, s25, 0x1c000
	v_lshl_add_u64 v[2:3], s[0:1], 0, v[130:131]
	global_load_lds_dwordx4 v[2:3], off
	v_lshl_add_u64 v[2:3], s[0:1], 0, v[132:133]
	s_add_i32 m0, s25, 0x1e000
	v_and_b32_e32 v1, 15, v6
	global_load_lds_dwordx4 v[2:3], off
	s_waitcnt vmcnt(8)
	s_barrier
	v_bfe_u32 v3, v6, 4, 2
	v_lshlrev_b32_e32 v3, 3, v3
	v_or_b32_e32 v14, s50, v3
	v_and_or_b32 v3, s14, 32, v3
	v_lshrrev_b32_e32 v144, 4, v3
	v_lshlrev_b32_e32 v3, 1, v6
	v_lshrrev_b32_e32 v2, 4, v6
	v_and_b32_e32 v5, 7, v6
	v_and_or_b32 v3, v3, 32, v1
	v_or_b32_e32 v4, s49, v1
	v_bitop3_b32 v2, v2, v5, 3 bitop3:0x6c
	v_or_b32_e32 v13, s50, v1
	v_lshlrev_b32_e32 v146, 4, v3
	v_lshlrev_b32_e32 v3, 10, v11
	v_lshlrev_b32_e32 v4, 7, v4
	v_lshlrev_b32_e32 v2, 4, v2
	v_lshlrev_b32_e32 v13, 7, v13
	s_cmpk_lt_u32 s12, 0x100
	v_lshl_add_u32 v3, v10, 13, v3
	v_or_b32_e32 v5, v4, v2
	v_or_b32_e32 v145, v13, v2
	s_cselect_b64 s[12:13], -1, 0
	v_bitop3_b32 v165, v13, 64, v2 bitop3:0x36
	v_bitop3_b32 v2, v4, 64, v2 bitop3:0x36
	v_or_b32_e32 v3, v3, v12
	v_mov_b32_e32 v4, 0x40000
	s_add_i32 s0, 0, 0x10800
	v_lshl_add_u32 v150, v3, 1, v4
	v_lshlrev_b32_e32 v3, 10, v8
	v_add_u32_e32 v168, s0, v145
	v_add_u32_e32 v169, s0, v165
	s_add_i32 s0, 0, 0x14800
	s_waitcnt vmcnt(6)
	v_lshl_add_u32 v3, v7, 13, v3
	v_add_u32_e32 v172, s0, v145
	v_add_u32_e32 v173, s0, v165
	s_add_i32 s0, 0, 0x18800
	v_or_b32_e32 v3, v3, v9
	s_add_i32 s56, 0, 0x10000
	s_add_i32 s57, 0, 0x14000
	v_add_u32_e32 v176, s0, v145
	v_add_u32_e32 v177, s0, v165
	s_add_i32 s0, 0, 0x1c800
	v_mov_b32_e32 v139, v143
	v_mov_b32_e32 v141, v143
	v_or_b32_e32 v164, 0xfffffa00, v14
	v_mov_b32_e32 v147, v143
	v_or_b32_e32 v148, 0x100, v146
	v_mov_b32_e32 v149, v143
	s_ashr_i32 s55, s33, 31
	v_mov_b32_e32 v151, v143
	v_lshl_add_u32 v152, v3, 1, v4
	v_mov_b32_e32 v153, v143
	v_mov_b64_e32 v[154:155], 0x18c
	v_mov_b64_e32 v[156:157], 0x18b
	v_add_u32_e32 v166, s56, v145
	v_add_u32_e32 v167, s56, v165
	v_add_u32_e32 v170, s57, v145
	v_add_u32_e32 v171, s57, v165
	v_add_u32_e32 v174, 0, v5
	v_add_u32_e32 v175, 0, v2
	v_add_u32_e32 v178, s0, v145
	v_add_u32_e32 v179, s0, v165
	s_mov_b32 s58, 0x28000
	s_mov_b64 s[14:15], 0x2c000
	s_mov_b32 s59, 0x2c000
	s_barrier
	s_branch .LBB0_185

; __device__ __forceinline__ int tidx() { int t = threadIdx.x; asm volatile("" : "+v"(t)); return t; }
; __host__ __device__ __forceinline__ int lds_byte(int r, int c) { return (r >> 3) * 1024 + (r & 7) * 128 + ((((c >> 3) ^ r) & 7) << 4) + (c & 7) * 2; }
; #define PG8_STAGE(bufoff, gbase, voff) do { _Pragma("unroll") for (int _i = 0; _i < 2; ++_i) \
;         __builtin_amdgcn_global_load_lds((const unsigned*)((const char*)(gbase) + (voff)[_i]), (LAS unsigned*)(lds + (bufoff) + ldsw + _i * 8192), 16, 0, 0); } while (0)
; #define PG8_WAIT_V(n) asm volatile("s_waitcnt vmcnt(" #n ")" ::: "memory")
; #define PG8_BAR __builtin_amdgcn_s_barrier()
;     const int tid = tidx(), wid = __builtin_amdgcn_readfirstlane(tid >> 6), lane = tid & 63, wr = wid >> 2, wc = wid & 3, fr = lane & 15, fq = lane >> 4;
;     const int K = (int)g.K, ntf = K / BK;
;     int sR[2], sC[2]; unsigned voffB[2], voffA[2][2], voffN[2][2];
; #pragma unroll
;     for (int i = 0; i < 2; ++i) { stage_rc(tid * 16 + i * 8192, sR[i], sC[i]); const int Rb = Epi::PERM ? ((sR[i] & ~31) + perm32(sR[i] & 31)) : sR[i];
;         voffB[i] = (TILED & 2) ? (unsigned)(Rb * BK + sC[i]) * 2u : (unsigned)(Rb * K + sC[i]) * 2u; }
;     constexpr size_t kstepA = (TILED & 1) ? (size_t)HALF * BK * 2 : (size_t)(BK * 2), kstepB = (TILED & 2) ? (size_t)HALF * BK * 2 : (size_t)(BK * 2);
;     const size_t hstep = (size_t)HALF * K * 2;
;     const size_t tstep = 2 * hstep;
;     const unsigned ldsw = (unsigned)wid * 1024u;
;     const int aoff = lds_byte(wr * 64 + fr, fq * 8), boff = lds_byte(wc * 32 + fr, fq * 8);
;     ...
;     const char* cA = (const char*)(g.A + (size_t)cur.z * g.aStrideZ) + (GATHER ? (size_t)0 : (size_t)cur.pm * tstep) + k0t(cur) * kstepA;
;     const char* cB = (const char*)(g.Bt + (size_t)cur.z * g.bStrideZ) + (size_t)cur.pn * tstep + k0t(cur) * kstepB;
;     PG8_STAGE(PG8_SB(0, 0), cB, voffB); PG8_STAGE(PG8_SB(0, 1), cB + hstep, voffB); PG8_STAGE(PG8_SA(0, 0), cA, voffA[0]); PG8_STAGE(PG8_SA(0, 1), cA, voffA[1]);
;     if (wr == 1) PG8_BAR;
;     PG8_WAIT_V(2); PG8_BAR;
;     PG8_STAGE(PG8_SB(1, 0), cB + kstepB, voffB); PG8_STAGE(PG8_SA(1, 0), cA + kstepA, voffA[0]); PG8_STAGE(PG8_SB(1, 1), cB + hstep + kstepB, voffB);
;     PG8_WAIT_V(6); PG8_BAR;
.LBB0_206:
	s_lshl_b32 s12, s12, 5
	s_lshl_b32 s57, s13, 6
	s_and_b32 s54, s12, 0x60
	s_mov_b64 s[12:13], 0x80
	s_add_i32 m0, s27, 0x18000
	v_lshl_add_u64 v[4:5], v[4:5], 0, s[12:13]
	global_load_lds_dwordx4 v[4:5], off
	s_add_i32 m0, s27, 0x1a000
	s_add_u32 s16, s30, 0x4000
	v_lshl_add_u64 v[2:3], v[2:3], 0, s[12:13]
	s_addc_u32 s17, s31, 0
	s_add_i32 s55, s27, 0x8000
	global_load_lds_dwordx4 v[2:3], off
	v_lshl_add_u64 v[2:3], s[16:17], 0, v[134:135]
	s_mov_b32 m0, s55
	s_add_i32 s56, s27, 0xa000
	global_load_lds_dwordx4 v[2:3], off
	v_lshl_add_u64 v[2:3], s[16:17], 0, v[136:137]
	s_add_u32 s16, s4, 0x40080
	s_mov_b32 m0, s56
	s_addc_u32 s17, s5, 0
	global_load_lds_dwordx4 v[2:3], off
	s_add_i32 m0, s27, 0x1c000
	v_lshl_add_u64 v[2:3], s[16:17], 0, v[132:133]
	global_load_lds_dwordx4 v[2:3], off
	v_lshl_add_u64 v[2:3], s[16:17], 0, v[130:131]
	s_add_i32 m0, s27, 0x1e000
	v_and_b32_e32 v13, 7, v7
	global_load_lds_dwordx4 v[2:3], off
	s_waitcnt vmcnt(8)
	s_barrier
	v_lshrrev_b32_e32 v2, 4, v7
	v_and_b32_e32 v3, 15, v7
	v_bitop3_b32 v2, v2, v13, 3 bitop3:0x6c
	v_lshlrev_b32_e32 v13, 4, v2
	v_or_b32_e32 v2, s54, v3
	v_lshlrev_b32_e32 v15, 7, v2
	v_lshlrev_b32_e32 v2, 1, v7
	v_and_or_b32 v142, v2, 64, v3
	v_lshrrev_b32_e32 v2, 1, v7
	v_or_b32_e32 v4, s57, v3
	v_and_b32_e32 v2, 8, v2
	v_mov_b32_e32 v3, v133
	v_lshl_add_u64 v[144:145], s[8:9], 0, v[2:3]
	v_lshlrev_b32_e32 v3, 7, v10
	s_cmpk_lt_u32 s14, 0x100
	v_lshl_add_u32 v3, v11, 10, v3
	v_or_b32_e32 v143, v15, v13
	s_cselect_b64 s[14:15], -1, 0
	v_bitop3_b32 v152, v15, 64, v13 bitop3:0x36
	v_or_b32_e32 v3, v3, v12
	s_add_i32 s16, 0, 0x10800
	v_add_u32_e32 v148, 0x40000, v3
	v_lshlrev_b32_e32 v3, 7, v8
	v_add_u32_e32 v155, s16, v143
	v_add_u32_e32 v156, s16, v152
	s_add_i32 s16, 0, 0x14800
	v_lshlrev_b32_e32 v5, 7, v4
	s_waitcnt vmcnt(6)
	v_lshl_add_u32 v3, v6, 10, v3
	v_add_u32_e32 v159, s16, v143
	v_add_u32_e32 v160, s16, v152
	s_add_i32 s16, 0, 0x18800
	v_bfe_u32 v1, v7, 4, 2
	v_or_b32_e32 v14, v5, v13
	v_bitop3_b32 v2, v5, 64, v13 bitop3:0x36
	v_or_b32_e32 v3, v3, v9
	s_add_i32 s58, 0, 0x10000
	s_add_i32 s59, 0, 0x14000
	v_add_u32_e32 v163, s16, v143
	v_add_u32_e32 v164, s16, v152
	s_add_i32 s16, 0, 0x1c800
	v_mov_b32_e32 v139, v133
	v_mov_b32_e32 v141, v133
	v_lshlrev_b32_e32 v1, 3, v1
	s_addk_i32 s57, 0xfc00
	v_or_b32_e32 v146, 16, v142
	v_add_u32_e32 v147, 0xfffff800, v4
	v_mov_b32_e32 v149, v133
	v_add_u32_e32 v150, 0x40000, v3
	v_mov_b32_e32 v151, v133
	v_add_u32_e32 v153, s58, v143
	v_add_u32_e32 v154, s58, v152
	v_add_u32_e32 v157, s59, v143
	v_add_u32_e32 v158, s59, v152
	v_add_u32_e32 v161, 0, v14
	v_add_u32_e32 v162, 0, v2
	v_add_u32_e32 v165, s16, v143
	v_add_u32_e32 v166, s16, v152
	s_mov_b32 s60, 0x8400
	s_barrier
	s_branch .LBB0_209

; __device__ __forceinline__ int tidx() { int t = threadIdx.x; asm volatile("" : "+v"(t)); return t; }
; __host__ __device__ __forceinline__ int lds_byte(int r, int c) { return (r >> 3) * 1024 + (r & 7) * 128 + ((((c >> 3) ^ r) & 7) << 4) + (c & 7) * 2; }
; #define PG8_STAGE(bufoff, gbase, voff) do { _Pragma("unroll") for (int _i = 0; _i < 2; ++_i) \
;         __builtin_amdgcn_global_load_lds((const unsigned*)((const char*)(gbase) + (voff)[_i]), (LAS unsigned*)(lds + (bufoff) + ldsw + _i * 8192), 16, 0, 0); } while (0)
; #define PG8_WAIT_V(n) asm volatile("s_waitcnt vmcnt(" #n ")" ::: "memory")
; #define PG8_BAR __builtin_amdgcn_s_barrier()
;     const int tid = tidx(), wid = __builtin_amdgcn_readfirstlane(tid >> 6), lane = tid & 63, wr = wid >> 2, wc = wid & 3, fr = lane & 15, fq = lane >> 4;
;     const int K = (int)g.K, ntf = K / BK;
;     int sR[2], sC[2]; unsigned voffB[2], voffA[2][2], voffN[2][2];
; #pragma unroll
;     for (int i = 0; i < 2; ++i) { stage_rc(tid * 16 + i * 8192, sR[i], sC[i]); const int Rb = Epi::PERM ? ((sR[i] & ~31) + perm32(sR[i] & 31)) : sR[i];
;         voffB[i] = (TILED & 2) ? (unsigned)(Rb * BK + sC[i]) * 2u : (unsigned)(Rb * K + sC[i]) * 2u; }
;     constexpr size_t kstepA = (TILED & 1) ? (size_t)HALF * BK * 2 : (size_t)(BK * 2), kstepB = (TILED & 2) ? (size_t)HALF * BK * 2 : (size_t)(BK * 2);
;     const size_t hstep = (size_t)HALF * K * 2;
;     const size_t tstep = 2 * hstep;
;     const unsigned ldsw = (unsigned)wid * 1024u;
;     const int aoff = lds_byte(wr * 64 + fr, fq * 8), boff = lds_byte(wc * 32 + fr, fq * 8);
;     ...
;     const char* cA = (const char*)(g.A + (size_t)cur.z * g.aStrideZ) + (GATHER ? (size_t)0 : (size_t)cur.pm * tstep) + k0t(cur) * kstepA;
;     const char* cB = (const char*)(g.Bt + (size_t)cur.z * g.bStrideZ) + (size_t)cur.pn * tstep + k0t(cur) * kstepB;
;     PG8_STAGE(PG8_SB(0, 0), cB, voffB); PG8_STAGE(PG8_SB(0, 1), cB + hstep, voffB); PG8_STAGE(PG8_SA(0, 0), cA, voffA[0]); PG8_STAGE(PG8_SA(0, 1), cA, voffA[1]);
;     if (wr == 1) PG8_BAR;
;     PG8_WAIT_V(2); PG8_BAR;
;     PG8_STAGE(PG8_SB(1, 0), cB + kstepB, voffB); PG8_STAGE(PG8_SA(1, 0), cA + kstepA, voffA[0]); PG8_STAGE(PG8_SB(1, 1), cB + hstep + kstepB, voffB);
;     PG8_WAIT_V(6); PG8_BAR;
.LBB0_450:
	s_and_b32 s54, s0, 3
	s_add_u32 s0, s2, 0x4000
	s_addc_u32 s1, s3, 0
	s_add_i32 m0, s50, 0x18000
	v_lshl_add_u64 v[12:13], s[0:1], 0, v[146:147]
	global_load_lds_dwordx4 v[12:13], off
	v_lshl_add_u64 v[12:13], s[0:1], 0, v[148:149]
	s_add_i32 m0, s50, 0x1a000
	s_mov_b64 s[92:93], 0x80
	s_add_i32 s55, s50, 0x8000
	s_add_i32 s56, s50, 0xa000
	global_load_lds_dwordx4 v[12:13], off
	v_lshl_add_u64 v[2:3], v[2:3], 0, s[92:93]
	s_mov_b32 m0, s55
	s_add_u32 s0, s2, 0x44000
	global_load_lds_dwordx4 v[2:3], off
	v_lshl_add_u64 v[2:3], v[4:5], 0, s[92:93]
	s_mov_b32 m0, s56
	s_addc_u32 s1, s3, 0
	global_load_lds_dwordx4 v[2:3], off
	s_add_i32 m0, s50, 0x1c000
	v_lshl_add_u64 v[2:3], s[0:1], 0, v[146:147]
	global_load_lds_dwordx4 v[2:3], off
	v_lshl_add_u64 v[2:3], s[0:1], 0, v[148:149]
	s_add_i32 m0, s50, 0x1e000
	s_cmpk_lt_u32 s6, 0x100
	global_load_lds_dwordx4 v[2:3], off
	s_waitcnt vmcnt(8)
	s_barrier
	s_cselect_b64 s[24:25], -1, 0
	s_ashr_i32 s57, s33, 31
	s_ashr_i32 s58, s94, 31
	s_mov_b32 s96, s94
	s_add_u32 s94, s90, 0x13600
	s_addc_u32 s95, s91, 0
	s_add_u32 s59, s90, 0x51a15600
	s_addc_u32 s60, s91, 0
	s_add_u32 s61, s90, 0x12a13600
	s_addc_u32 s62, s91, 0
	s_add_u32 s63, s90, 0x3600
	s_addc_u32 s64, s91, 0
	s_add_u32 s0, s90, 0x51a37600
	v_lshrrev_b32_e32 v2, 4, v1
	v_and_b32_e32 v199, 15, v1
	v_and_b32_e32 v5, 7, v1
	s_addc_u32 s1, s91, 0
	v_lshlrev_b32_e32 v3, 7, v199
	v_bitop3_b32 v2, v2, v5, 3 bitop3:0x6c
	v_writelane_b32 v250, s0, 34
	v_lshl_or_b32 v4, s48, 13, v3
	v_lshlrev_b32_e32 v2, 4, v2
	v_lshl_or_b32 v3, s54, 12, v3
	v_writelane_b32 v250, s1, 35
	s_add_u32 s0, s90, 0x51b37600
	v_or_b32_e32 v201, v3, v2
	v_bitop3_b32 v202, v3, 64, v2 bitop3:0x36
	s_addc_u32 s1, s91, 0
	v_lshlrev_b32_e32 v3, 10, v10
	v_writelane_b32 v250, s0, 36
	v_lshl_add_u32 v3, v9, 13, v3
	v_or_b32_e32 v5, v2, v4
	v_bitop3_b32 v2, v2, 64, v4 bitop3:0x36
	v_writelane_b32 v250, s1, 37
	v_or_b32_e32 v3, v3, v11
	v_mov_b32_e32 v4, 0x40000
	s_add_i32 s0, 0, 0x10800
	v_lshl_add_u32 v160, v3, 1, v4
	v_lshlrev_b32_e32 v3, 10, v7
	v_add_u32_e32 v205, s0, v201
	v_add_u32_e32 v206, s0, v202
	s_add_i32 s0, 0, 0x14800
	s_waitcnt vmcnt(6)
	v_lshl_add_u32 v3, v6, 13, v3
	v_add_u32_e32 v209, s0, v201
	v_add_u32_e32 v210, s0, v202
	s_add_i32 s0, 0, 0x18800
	v_or_b32_e32 v3, v3, v8
	s_add_i32 s65, 0, 0x10000
	s_add_i32 s66, 0, 0x14000
	v_add_u32_e32 v213, s0, v201
	v_add_u32_e32 v214, s0, v202
	s_add_i32 s0, 0, 0x1c800
	v_mov_b32_e32 v155, v159
	v_mov_b32_e32 v157, v159
	v_bfe_u32 v200, v1, 4, 2
	v_mov_b32_e32 v161, v159
	v_lshl_add_u32 v162, v3, 1, v4
	v_mov_b32_e32 v163, v159
	v_mov_b64_e32 v[164:165], 0x100
	v_mov_b64_e32 v[166:167], 0xff
	v_add_u32_e32 v203, s65, v201
	v_add_u32_e32 v204, s65, v202
	v_add_u32_e32 v207, s66, v201
	v_add_u32_e32 v208, s66, v202
	v_add_u32_e32 v211, 0, v5
	v_add_u32_e32 v212, 0, v2
	v_add_u32_e32 v215, s0, v201
	v_add_u32_e32 v216, s0, v202
	s_movk_i32 s67, 0x7fff
	s_add_i32 s68, 0, 0x4300
	s_movk_i32 s69, 0x140
	s_add_i32 s70, 0, 0x19700
	v_mov_b32_e32 v217, 0x358637bd
	s_mov_b32 s71, 0x3fb8aa3b
	s_mov_b32 s72, 0xc2ce8ed0
	s_mov_b32 s73, 0x42b17218
	v_mov_b32_e32 v218, 0x7f800000
	v_mov_b32_e32 v219, 0x7fc00000
	s_mov_b32 s75, 0
	s_barrier
	s_branch .LBB0_453

; __device__ __forceinline__ int tidx() { int t = threadIdx.x; asm volatile("" : "+v"(t)); return t; }
; __host__ __device__ __forceinline__ int lds_byte(int r, int c) { return (r >> 3) * 1024 + (r & 7) * 128 + ((((c >> 3) ^ r) & 7) << 4) + (c & 7) * 2; }
; #define PG8_STAGE(bufoff, gbase, voff) do { _Pragma("unroll") for (int _i = 0; _i < 2; ++_i) \
;         __builtin_amdgcn_global_load_lds((const unsigned*)((const char*)(gbase) + (voff)[_i]), (LAS unsigned*)(lds + (bufoff) + ldsw + _i * 8192), 16, 0, 0); } while (0)
; #define PG8_WAIT_V(n) asm volatile("s_waitcnt vmcnt(" #n ")" ::: "memory")
; #define PG8_BAR __builtin_amdgcn_s_barrier()
;     const int tid = tidx(), wid = __builtin_amdgcn_readfirstlane(tid >> 6), lane = tid & 63, wr = wid >> 2, wc = wid & 3, fr = lane & 15, fq = lane >> 4;
;     const int K = (int)g.K, ntf = K / BK;
;     int sR[2], sC[2]; unsigned voffB[2], voffA[2][2], voffN[2][2];
; #pragma unroll
;     for (int i = 0; i < 2; ++i) { stage_rc(tid * 16 + i * 8192, sR[i], sC[i]); const int Rb = Epi::PERM ? ((sR[i] & ~31) + perm32(sR[i] & 31)) : sR[i];
;         voffB[i] = (TILED & 2) ? (unsigned)(Rb * BK + sC[i]) * 2u : (unsigned)(Rb * K + sC[i]) * 2u; }
;     constexpr size_t kstepA = (TILED & 1) ? (size_t)HALF * BK * 2 : (size_t)(BK * 2), kstepB = (TILED & 2) ? (size_t)HALF * BK * 2 : (size_t)(BK * 2);
;     const size_t hstep = (size_t)HALF * K * 2;
;     const size_t tstep = 2 * hstep;
;     const unsigned ldsw = (unsigned)wid * 1024u;
;     const int aoff = lds_byte(wr * 64 + fr, fq * 8), boff = lds_byte(wc * 32 + fr, fq * 8);
;     ...
;     const char* cA = (const char*)(g.A + (size_t)cur.z * g.aStrideZ) + (GATHER ? (size_t)0 : (size_t)cur.pm * tstep) + k0t(cur) * kstepA;
;     const char* cB = (const char*)(g.Bt + (size_t)cur.z * g.bStrideZ) + (size_t)cur.pn * tstep + k0t(cur) * kstepB;
;     PG8_STAGE(PG8_SB(0, 0), cB, voffB); PG8_STAGE(PG8_SB(0, 1), cB + hstep, voffB); PG8_STAGE(PG8_SA(0, 0), cA, voffA[0]); PG8_STAGE(PG8_SA(0, 1), cA, voffA[1]);
;     if (wr == 1) PG8_BAR;
;     PG8_WAIT_V(2); PG8_BAR;
;     PG8_STAGE(PG8_SB(1, 0), cB + kstepB, voffB); PG8_STAGE(PG8_SA(1, 0), cA + kstepA, voffA[0]); PG8_STAGE(PG8_SB(1, 1), cB + hstep + kstepB, voffB);
;     PG8_WAIT_V(6); PG8_BAR;
.LBB0_551:
	s_and_b32 s54, s5, 3
	s_add_u32 s14, s0, 0x4000
	s_addc_u32 s15, s1, 0
	s_add_i32 m0, s50, 0x18000
	v_lshl_add_u64 v[12:13], s[14:15], 0, v[146:147]
	global_load_lds_dwordx4 v[12:13], off
	v_lshl_add_u64 v[12:13], s[14:15], 0, v[148:149]
	s_add_i32 m0, s50, 0x1a000
	s_mov_b64 s[92:93], 0x80
	s_add_i32 s55, s50, 0x8000
	s_add_i32 s56, s50, 0xa000
	global_load_lds_dwordx4 v[12:13], off
	v_lshl_add_u64 v[2:3], v[2:3], 0, s[92:93]
	s_mov_b32 m0, s55
	s_add_u32 s16, s0, 0x44000
	global_load_lds_dwordx4 v[2:3], off
	v_lshl_add_u64 v[2:3], v[4:5], 0, s[92:93]
	s_mov_b32 m0, s56
	s_addc_u32 s17, s1, 0
	global_load_lds_dwordx4 v[2:3], off
	s_add_i32 m0, s50, 0x1c000
	v_lshl_add_u64 v[2:3], s[16:17], 0, v[146:147]
	global_load_lds_dwordx4 v[2:3], off
	v_lshl_add_u64 v[2:3], s[16:17], 0, v[148:149]
	s_add_i32 m0, s50, 0x1e000
	s_cmpk_lt_u32 s4, 0x100
	global_load_lds_dwordx4 v[2:3], off
	s_waitcnt vmcnt(8)
	s_barrier
	s_cselect_b64 s[80:81], -1, 0
	s_add_u32 s96, s90, 0x13600
	s_addc_u32 s97, s91, 0
	s_add_u32 s57, s90, 0x51a15600
	s_addc_u32 s58, s91, 0
	s_add_u32 s59, s90, 0x12a13600
	s_addc_u32 s60, s91, 0
	s_add_u32 s61, s90, 0x3600
	s_addc_u32 s62, s91, 0
	s_add_u32 s4, s90, 0x51a37600
	v_lshrrev_b32_e32 v2, 4, v1
	v_and_b32_e32 v194, 15, v1
	v_and_b32_e32 v5, 7, v1
	s_addc_u32 s5, s91, 0
	v_lshlrev_b32_e32 v3, 7, v194
	v_bitop3_b32 v2, v2, v5, 3 bitop3:0x6c
	v_writelane_b32 v250, s4, 34
	v_lshl_or_b32 v4, s48, 13, v3
	v_lshlrev_b32_e32 v2, 4, v2
	v_lshl_or_b32 v3, s54, 12, v3
	v_writelane_b32 v250, s5, 35
	s_add_u32 s4, s90, 0x51b37600
	v_or_b32_e32 v196, v3, v2
	v_bitop3_b32 v197, v3, 64, v2 bitop3:0x36
	s_addc_u32 s5, s91, 0
	v_lshlrev_b32_e32 v3, 10, v10
	v_writelane_b32 v250, s4, 36
	v_lshl_add_u32 v3, v9, 13, v3
	v_or_b32_e32 v5, v2, v4
	v_bitop3_b32 v2, v2, 64, v4 bitop3:0x36
	v_writelane_b32 v250, s5, 37
	v_or_b32_e32 v3, v3, v11
	v_mov_b32_e32 v4, 0x40000
	s_add_i32 s4, 0, 0x10800
	v_lshl_add_u32 v160, v3, 1, v4
	v_lshlrev_b32_e32 v3, 10, v7
	v_add_u32_e32 v201, s4, v196
	v_add_u32_e32 v202, s4, v197
	s_add_i32 s4, 0, 0x14800
	s_waitcnt vmcnt(6)
	v_lshl_add_u32 v3, v6, 13, v3
	v_add_u32_e32 v205, s4, v196
	v_add_u32_e32 v206, s4, v197
	s_add_i32 s4, 0, 0x18800
	v_or_b32_e32 v3, v3, v8
	s_add_i32 s63, 0, 0x10000
	s_add_i32 s64, 0, 0x14000
	v_add_u32_e32 v209, s4, v196
	v_add_u32_e32 v210, s4, v197
	s_add_i32 s4, 0, 0x1c800
	v_mov_b32_e32 v155, v159
	v_mov_b32_e32 v157, v159
	v_bfe_u32 v195, v1, 4, 2
	v_mov_b32_e32 v161, v159
	v_lshl_add_u32 v162, v3, 1, v4
	v_mov_b32_e32 v163, v159
	v_add_u32_e32 v199, s63, v196
	v_add_u32_e32 v200, s63, v197
	v_add_u32_e32 v203, s64, v196
	v_add_u32_e32 v204, s64, v197
	v_add_u32_e32 v207, 0, v5
	v_add_u32_e32 v208, 0, v2
	v_add_u32_e32 v211, s4, v196
	v_add_u32_e32 v212, s4, v197
	s_movk_i32 s65, 0x7fff
	s_add_i32 s66, 0, 0x4300
	s_movk_i32 s67, 0x140
	s_add_i32 s68, 0, 0x19700
	v_mov_b32_e32 v213, 0x358637bd
	s_mov_b32 s69, 0x3fb8aa3b
	s_mov_b32 s70, 0xc2ce8ed0
	s_mov_b32 s71, 0x42b17218
	v_mov_b32_e32 v214, 0x7f800000
	v_mov_b32_e32 v215, 0x7fc00000
	s_mov_b32 s72, 0
	s_barrier
	s_branch .LBB0_554

; __device__ __forceinline__ int tidx() { int t = threadIdx.x; asm volatile("" : "+v"(t)); return t; }
; __host__ __device__ __forceinline__ int lds_byte(int r, int c) { return (r >> 3) * 1024 + (r & 7) * 128 + ((((c >> 3) ^ r) & 7) << 4) + (c & 7) * 2; }
; #define PG8_STAGE(bufoff, gbase, voff) do { _Pragma("unroll") for (int _i = 0; _i < 2; ++_i) \
;         __builtin_amdgcn_global_load_lds((const unsigned*)((const char*)(gbase) + (voff)[_i]), (LAS unsigned*)(lds + (bufoff) + ldsw + _i * 8192), 16, 0, 0); } while (0)
; #define PG8_WAIT_V(n) asm volatile("s_waitcnt vmcnt(" #n ")" ::: "memory")
; #define PG8_BAR __builtin_amdgcn_s_barrier()
;     const int tid = tidx(), wid = __builtin_amdgcn_readfirstlane(tid >> 6), lane = tid & 63, wr = wid >> 2, wc = wid & 3, fr = lane & 15, fq = lane >> 4;
;     const int K = (int)g.K, ntf = K / BK;
;     int sR[2], sC[2]; unsigned voffB[2], voffA[2][2], voffN[2][2];
; #pragma unroll
;     for (int i = 0; i < 2; ++i) { stage_rc(tid * 16 + i * 8192, sR[i], sC[i]); const int Rb = Epi::PERM ? ((sR[i] & ~31) + perm32(sR[i] & 31)) : sR[i];
;         voffB[i] = (TILED & 2) ? (unsigned)(Rb * BK + sC[i]) * 2u : (unsigned)(Rb * K + sC[i]) * 2u; }
;     constexpr size_t kstepA = (TILED & 1) ? (size_t)HALF * BK * 2 : (size_t)(BK * 2), kstepB = (TILED & 2) ? (size_t)HALF * BK * 2 : (size_t)(BK * 2);
;     const size_t hstep = (size_t)HALF * K * 2;
;     const size_t tstep = 2 * hstep;
;     const unsigned ldsw = (unsigned)wid * 1024u;
;     const int aoff = lds_byte(wr * 64 + fr, fq * 8), boff = lds_byte(wc * 32 + fr, fq * 8);
;     ...
;     const char* cA = (const char*)(g.A + (size_t)cur.z * g.aStrideZ) + (GATHER ? (size_t)0 : (size_t)cur.pm * tstep) + k0t(cur) * kstepA;
;     const char* cB = (const char*)(g.Bt + (size_t)cur.z * g.bStrideZ) + (size_t)cur.pn * tstep + k0t(cur) * kstepB;
;     PG8_STAGE(PG8_SB(0, 0), cB, voffB); PG8_STAGE(PG8_SB(0, 1), cB + hstep, voffB); PG8_STAGE(PG8_SA(0, 0), cA, voffA[0]); PG8_STAGE(PG8_SA(0, 1), cA, voffA[1]);
;     if (wr == 1) PG8_BAR;
;     PG8_WAIT_V(2); PG8_BAR;
;     PG8_STAGE(PG8_SB(1, 0), cB + kstepB, voffB); PG8_STAGE(PG8_SA(1, 0), cA + kstepA, voffA[0]); PG8_STAGE(PG8_SB(1, 1), cB + hstep + kstepB, voffB);
;     PG8_WAIT_V(6); PG8_BAR;
.LBB0_997:
	s_lshl_b32 s45, s1, 6
	s_lshl_b32 s1, s0, 5
	s_and_b32 s46, s1, 0x60
	s_add_u32 s8, s6, 0x4000
	s_addc_u32 s9, s7, 0
	s_add_i32 s47, s23, 0x18000
	s_add_i32 s48, s23, 0x1a000
	v_lshl_add_u64 v[8:9], s[8:9], 0, v[202:203]
	s_mov_b32 m0, s47
	s_add_u32 s12, s90, 0x4213680
	global_load_lds_dwordx4 v[8:9], off
	v_lshl_add_u64 v[8:9], s[8:9], 0, v[204:205]
	s_mov_b32 m0, s48
	s_addc_u32 s13, s91, 0
	s_add_i32 s49, s23, 0x8000
	s_add_i32 s50, s23, 0xa000
	global_load_lds_dwordx4 v[8:9], off
	v_lshl_add_u64 v[8:9], s[12:13], 0, v[2:3]
	s_mov_b32 m0, s49
	s_add_u32 s8, s6, 0x44000
	global_load_lds_dwordx4 v[8:9], off
	v_lshl_add_u64 v[4:5], s[12:13], 0, v[4:5]
	s_mov_b32 m0, s50
	s_addc_u32 s9, s7, 0
	s_add_i32 s51, s23, 0x1c000
	global_load_lds_dwordx4 v[4:5], off
	v_lshl_add_u64 v[4:5], s[8:9], 0, v[202:203]
	s_mov_b32 m0, s51
	s_add_i32 s52, s23, 0x1e000
	global_load_lds_dwordx4 v[4:5], off
	v_lshl_add_u64 v[4:5], s[8:9], 0, v[204:205]
	s_mov_b32 m0, s52
	v_lshrrev_b32_e32 v2, 4, v6
	global_load_lds_dwordx4 v[4:5], off
	s_waitcnt vmcnt(8)
	s_barrier
	v_and_b32_e32 v4, 15, v6
	v_bfe_u32 v5, v6, 4, 2
	v_and_b32_e32 v6, 7, v6
	s_cmpk_lt_u32 s4, 0x100
	v_bitop3_b32 v2, v2, v6, 3 bitop3:0x6c
	s_cselect_b64 s[14:15], -1, 0
	s_lshl_b32 s0, s0, 6
	v_lshlrev_b32_e32 v8, 4, v2
	v_or_b32_e32 v2, s46, v4
	s_and_b32 s0, s0, 64
	v_lshlrev_b32_e32 v10, 7, v2
	v_lshl_or_b32 v2, v5, 4, s0
	v_readlane_b32 s0, v250, 32
	v_or_b32_e32 v7, s45, v4
	v_and_or_b32 v4, s45, 64, v4
	v_readlane_b32 s1, v250, 33
	v_lshlrev_b32_e32 v7, 7, v7
	s_waitcnt vmcnt(6)
	v_or_b32_e32 v9, v7, v8
	v_lshl_add_u64 v[206:207], s[0:1], 0, v[2:3]
	v_lshlrev_b32_e32 v2, 6, v4
	v_or_b32_e32 v4, 0x800, v2
	v_or_b32_e32 v6, 0xc00, v2
	v_bitop3_b32 v5, v7, 64, v8 bitop3:0x36
	s_lshl_b32 s0, s94, 1
	v_or_b32_e32 v226, v10, v8
	v_bitop3_b32 v227, v10, 64, v8 bitop3:0x36
	s_and_b32 s53, s0, 14
	s_add_i32 s54, 0, 0x10000
	s_add_i32 s55, 0, 0x10800
	s_add_i32 s56, 0, 0x14000
	s_add_i32 s57, 0, 0x14800
	s_add_i32 s58, 0, 0x18800
	s_add_i32 s59, 0, 0x1c800
	s_mov_b64 s[16:17], 0x80
	v_lshlrev_b32_e32 v208, 1, v2
	v_lshlrev_b32_e32 v210, 1, v4
	v_lshlrev_b32_e32 v212, 1, v6
	v_add_u32_e32 v228, 0, v9
	v_add_u32_e32 v229, 0, v5
	v_mov_b32_e32 v230, 0xc60000
	s_barrier
	s_branch .LBB0_1000

; __device__ __forceinline__ int tidx() { int t = threadIdx.x; asm volatile("" : "+v"(t)); return t; }
; __host__ __device__ __forceinline__ int lds_byte(int r, int c) { return (r >> 3) * 1024 + (r & 7) * 128 + ((((c >> 3) ^ r) & 7) << 4) + (c & 7) * 2; }
; #define PG8_STAGE(bufoff, gbase, voff) do { _Pragma("unroll") for (int _i = 0; _i < 2; ++_i) \
;         __builtin_amdgcn_global_load_lds((const unsigned*)((const char*)(gbase) + (voff)[_i]), (LAS unsigned*)(lds + (bufoff) + ldsw + _i * 8192), 16, 0, 0); } while (0)
; #define PG8_WAIT_V(n) asm volatile("s_waitcnt vmcnt(" #n ")" ::: "memory")
; #define PG8_BAR __builtin_amdgcn_s_barrier()
;     const int tid = tidx(), wid = __builtin_amdgcn_readfirstlane(tid >> 6), lane = tid & 63, wr = wid >> 2, wc = wid & 3, fr = lane & 15, fq = lane >> 4;
;     const int K = (int)g.K, ntf = K / BK;
;     int sR[2], sC[2]; unsigned voffB[2], voffA[2][2], voffN[2][2];
; #pragma unroll
;     for (int i = 0; i < 2; ++i) { stage_rc(tid * 16 + i * 8192, sR[i], sC[i]); const int Rb = Epi::PERM ? ((sR[i] & ~31) + perm32(sR[i] & 31)) : sR[i];
;         voffB[i] = (TILED & 2) ? (unsigned)(Rb * BK + sC[i]) * 2u : (unsigned)(Rb * K + sC[i]) * 2u; }
;     constexpr size_t kstepA = (TILED & 1) ? (size_t)HALF * BK * 2 : (size_t)(BK * 2), kstepB = (TILED & 2) ? (size_t)HALF * BK * 2 : (size_t)(BK * 2);
;     const size_t hstep = (size_t)HALF * K * 2;
;     const size_t tstep = 2 * hstep;
;     const unsigned ldsw = (unsigned)wid * 1024u;
;     const int aoff = lds_byte(wr * 64 + fr, fq * 8), boff = lds_byte(wc * 32 + fr, fq * 8);
;     ...
;     const char* cA = (const char*)(g.A + (size_t)cur.z * g.aStrideZ) + (GATHER ? (size_t)0 : (size_t)cur.pm * tstep) + k0t(cur) * kstepA;
;     const char* cB = (const char*)(g.Bt + (size_t)cur.z * g.bStrideZ) + (size_t)cur.pn * tstep + k0t(cur) * kstepB;
;     PG8_STAGE(PG8_SB(0, 0), cB, voffB); PG8_STAGE(PG8_SB(0, 1), cB + hstep, voffB); PG8_STAGE(PG8_SA(0, 0), cA, voffA[0]); PG8_STAGE(PG8_SA(0, 1), cA, voffA[1]);
;     if (wr == 1) PG8_BAR;
;     PG8_WAIT_V(2); PG8_BAR;
;     PG8_STAGE(PG8_SB(1, 0), cB + kstepB, voffB); PG8_STAGE(PG8_SA(1, 0), cA + kstepA, voffA[0]); PG8_STAGE(PG8_SB(1, 1), cB + hstep + kstepB, voffB);
;     PG8_WAIT_V(6); PG8_BAR;
.LBB0_1083:
	s_lshl_b32 s0, s5, 5
	s_and_b32 s5, s0, 0x60
	s_add_u32 s0, s8, 0x4000
	s_addc_u32 s1, s9, 0
	s_add_i32 s39, s28, 0x18000
	v_lshl_add_u64 v[10:11], s[0:1], 0, v[208:209]
	s_mov_b32 m0, s39
	s_add_i32 s40, s28, 0x1a000
	global_load_lds_dwordx4 v[10:11], off
	v_lshl_add_u64 v[10:11], s[0:1], 0, v[210:211]
	s_add_u32 s0, s6, 0x4000
	s_mov_b32 m0, s40
	s_addc_u32 s1, s7, 0
	s_add_i32 s41, s28, 0x8000
	global_load_lds_dwordx4 v[10:11], off
	v_lshl_add_u64 v[10:11], s[0:1], 0, v[200:201]
	s_mov_b32 m0, s41
	s_add_i32 s42, s28, 0xa000
	global_load_lds_dwordx4 v[10:11], off
	v_lshl_add_u64 v[10:11], s[0:1], 0, v[202:203]
	s_add_u32 s0, s8, 0xb4000
	s_mov_b32 m0, s42
	s_addc_u32 s1, s9, 0
	s_add_i32 s43, s28, 0x1c000
	global_load_lds_dwordx4 v[10:11], off
	v_lshl_add_u64 v[10:11], s[0:1], 0, v[208:209]
	s_mov_b32 m0, s43
	s_add_i32 s44, s28, 0x1e000
	global_load_lds_dwordx4 v[10:11], off
	v_lshl_add_u64 v[10:11], s[0:1], 0, v[210:211]
	s_mov_b32 m0, s44
	v_bfe_u32 v12, v3, 4, 2
	global_load_lds_dwordx4 v[10:11], off
	s_waitcnt vmcnt(8)
	s_barrier
	v_lshrrev_b32_e32 v10, 4, v3
	v_and_b32_e32 v11, 15, v3
	v_and_b32_e32 v3, 7, v3
	s_ashr_i32 s46, s33, 3
	v_lshl_or_b32 v1, s4, 6, v11
	v_bitop3_b32 v3, v10, v3, 3 bitop3:0x6c
	v_or_b32_e32 v11, s5, v11
	s_cmpk_lt_u32 s10, 0x100
	v_lshlrev_b32_e32 v5, 7, v5
	v_lshlrev_b32_e32 v3, 4, v3
	v_lshlrev_b32_e32 v11, 7, v11
	s_cselect_b64 s[10:11], -1, 0
	s_lshl_b32 s0, s94, 1
	v_lshl_add_u32 v4, v4, 10, v5
	v_or_b32_e32 v199, v11, v3
	s_and_b32 s47, s0, 14
	v_bitop3_b32 v216, v11, 64, v3 bitop3:0x36
	v_or_b32_e32 v4, v4, v6
	s_add_i32 s0, 0, 0x10000
	v_add_u32_e32 v212, 0xb0000, v4
	v_lshlrev_b32_e32 v4, 7, v8
	v_add_u32_e32 v218, s0, v199
	v_add_u32_e32 v219, s0, v216
	s_add_i32 s0, 0, 0x10800
	v_lshlrev_b32_e32 v13, 7, v1
	s_waitcnt vmcnt(6)
	v_lshl_add_u32 v4, v7, 10, v4
	v_add_u32_e32 v220, s0, v199
	v_add_u32_e32 v221, s0, v216
	s_add_i32 s0, 0, 0x14000
	v_or_b32_e32 v10, v13, v3
	v_bitop3_b32 v3, v13, 64, v3 bitop3:0x36
	v_or_b32_e32 v4, v4, v9
	v_add_u32_e32 v222, s0, v199
	v_add_u32_e32 v223, s0, v216
	s_add_i32 s0, 0, 0x14800
	v_mov_b32_e32 v205, v2
	v_mov_b32_e32 v207, v2
	v_lshl_or_b32 v217, v12, 3, s5
	v_mov_b32_e32 v213, v2
	v_add_u32_e32 v214, 0xb0000, v4
	v_mov_b32_e32 v215, v2
	v_add_u32_e32 v224, s0, v199
	v_add_u32_e32 v225, s0, v216
	v_add_u32_e32 v226, 0, v10
	v_add_u32_e32 v227, 0, v3
	s_add_i32 s48, 0, 0x18800
	s_add_i32 s49, 0, 0x1c800
	s_mov_b32 s50, 0x50000
	s_mov_b64 s[12:13], 0x58000
	s_mov_b32 s51, 0x58000
	s_barrier
	s_branch .LBB0_1086

; __device__ __forceinline__ int tidx() { int t = threadIdx.x; asm volatile("" : "+v"(t)); return t; }
; __host__ __device__ __forceinline__ int lds_byte(int r, int c) { return (r >> 3) * 1024 + (r & 7) * 128 + ((((c >> 3) ^ r) & 7) << 4) + (c & 7) * 2; }
; #define PG8_STAGE(bufoff, gbase, voff) do { _Pragma("unroll") for (int _i = 0; _i < 2; ++_i) \
;         __builtin_amdgcn_global_load_lds((const unsigned*)((const char*)(gbase) + (voff)[_i]), (LAS unsigned*)(lds + (bufoff) + ldsw + _i * 8192), 16, 0, 0); } while (0)
; #define PG8_WAIT_V(n) asm volatile("s_waitcnt vmcnt(" #n ")" ::: "memory")
; #define PG8_BAR __builtin_amdgcn_s_barrier()
;     const int tid = tidx(), wid = __builtin_amdgcn_readfirstlane(tid >> 6), lane = tid & 63, wr = wid >> 2, wc = wid & 3, fr = lane & 15, fq = lane >> 4;
;     const int K = (int)g.K, ntf = K / BK;
;     int sR[2], sC[2]; unsigned voffB[2], voffA[2][2], voffN[2][2];
; #pragma unroll
;     for (int i = 0; i < 2; ++i) { stage_rc(tid * 16 + i * 8192, sR[i], sC[i]); const int Rb = Epi::PERM ? ((sR[i] & ~31) + perm32(sR[i] & 31)) : sR[i];
;         voffB[i] = (TILED & 2) ? (unsigned)(Rb * BK + sC[i]) * 2u : (unsigned)(Rb * K + sC[i]) * 2u; }
;     constexpr size_t kstepA = (TILED & 1) ? (size_t)HALF * BK * 2 : (size_t)(BK * 2), kstepB = (TILED & 2) ? (size_t)HALF * BK * 2 : (size_t)(BK * 2);
;     const size_t hstep = (size_t)HALF * K * 2;
;     const size_t tstep = 2 * hstep;
;     const unsigned ldsw = (unsigned)wid * 1024u;
;     const int aoff = lds_byte(wr * 64 + fr, fq * 8), boff = lds_byte(wc * 32 + fr, fq * 8);
;     ...
;     const char* cA = (const char*)(g.A + (size_t)cur.z * g.aStrideZ) + (GATHER ? (size_t)0 : (size_t)cur.pm * tstep) + k0t(cur) * kstepA;
;     const char* cB = (const char*)(g.Bt + (size_t)cur.z * g.bStrideZ) + (size_t)cur.pn * tstep + k0t(cur) * kstepB;
;     PG8_STAGE(PG8_SB(0, 0), cB, voffB); PG8_STAGE(PG8_SB(0, 1), cB + hstep, voffB); PG8_STAGE(PG8_SA(0, 0), cA, voffA[0]); PG8_STAGE(PG8_SA(0, 1), cA, voffA[1]);
;     if (wr == 1) PG8_BAR;
;     PG8_WAIT_V(2); PG8_BAR;
;     PG8_STAGE(PG8_SB(1, 0), cB + kstepB, voffB); PG8_STAGE(PG8_SA(1, 0), cA + kstepA, voffA[0]); PG8_STAGE(PG8_SB(1, 1), cB + hstep + kstepB, voffB);
;     PG8_WAIT_V(6); PG8_BAR;
.LBB0_1251:
	s_and_b32 s3, s9, 3
	s_lshl_b32 s51, s6, 6
	s_lshl_b32 s11, s3, 5
	s_add_u32 s6, s38, 0x4000
	s_addc_u32 s7, s39, 0
	s_add_i32 m0, s47, 0x18000
	v_lshl_add_u64 v[14:15], s[6:7], 0, v[130:131]
	global_load_lds_dwordx4 v[14:15], off
	v_lshl_add_u64 v[14:15], s[6:7], 0, v[132:133]
	s_add_i32 m0, s47, 0x1a000
	s_mov_b64 s[20:21], 0x80
	s_add_i32 s52, s47, 0x8000
	s_add_i32 s53, s47, 0xa000
	global_load_lds_dwordx4 v[14:15], off
	v_lshl_add_u64 v[2:3], v[2:3], 0, s[20:21]
	s_mov_b32 m0, s52
	s_add_u32 s6, s38, 0x44000
	global_load_lds_dwordx4 v[2:3], off
	v_lshl_add_u64 v[2:3], v[4:5], 0, s[20:21]
	s_mov_b32 m0, s53
	s_addc_u32 s7, s39, 0
	global_load_lds_dwordx4 v[2:3], off
	s_add_i32 m0, s47, 0x1c000
	v_lshl_add_u64 v[2:3], s[6:7], 0, v[130:131]
	global_load_lds_dwordx4 v[2:3], off
	v_lshl_add_u64 v[2:3], s[6:7], 0, v[132:133]
	s_add_i32 m0, s47, 0x1e000
	v_lshrrev_b32_e32 v13, 4, v6
	global_load_lds_dwordx4 v[2:3], off
	s_waitcnt vmcnt(8)
	s_barrier
	v_and_b32_e32 v1, 15, v6
	v_and_b32_e32 v4, 7, v6
	s_cmpk_lt_u32 s8, 0x100
	v_bfe_u32 v2, v6, 4, 2
	v_or_b32_e32 v3, s51, v1
	v_bitop3_b32 v4, v13, v4, 3 bitop3:0x6c
	v_or_b32_e32 v6, s11, v1
	s_cselect_b64 s[22:23], -1, 0
	s_cmp_lt_u32 s3, 2
	v_lshlrev_b32_e32 v3, 7, v3
	v_lshlrev_b32_e32 v4, 4, v4
	v_lshlrev_b32_e32 v6, 7, v6
	s_cselect_b64 s[6:7], -1, 0
	s_ashr_i32 s54, s33, 31
	s_ashr_i32 s55, s94, 31
	s_lshl_b32 s3, s3, 10
	v_or_b32_e32 v5, v3, v4
	v_or_b32_e32 v170, v6, v4
	v_bitop3_b32 v174, v6, 64, v4 bitop3:0x36
	v_bitop3_b32 v3, v3, 64, v4 bitop3:0x36
	s_add_u32 s24, s90, s3
	v_lshlrev_b32_e32 v4, 4, v1
	s_addc_u32 s25, s91, 0
	v_lshl_or_b32 v142, v2, 8, v4
	s_lshl_b32 s3, s9, 8
	v_lshl_add_u64 v[144:145], s[24:25], 0, v[142:143]
	s_and_b32 s3, s3, 0x100
	v_lshlrev_b32_e32 v142, 6, v2
	v_lshl_or_b32 v175, v2, 3, s11
	v_lshlrev_b32_e32 v2, 10, v11
	s_add_u32 s8, s14, s3
	v_lshl_add_u32 v2, v10, 13, v2
	s_addc_u32 s9, s15, 0
	v_or_b32_e32 v2, v2, v12
	v_mov_b32_e32 v4, 0x40000
	s_add_i32 s3, 0, 0x10800
	v_lshl_add_u32 v148, v2, 1, v4
	v_lshlrev_b32_e32 v2, 10, v8
	v_add_u32_e32 v178, s3, v170
	v_add_u32_e32 v179, s3, v174
	s_add_i32 s3, 0, 0x14800
	s_waitcnt vmcnt(6)
	v_lshl_add_u32 v2, v7, 13, v2
	v_add_u32_e32 v182, s3, v170
	v_add_u32_e32 v183, s3, v174
	s_add_i32 s3, 0, 0x18800
	v_or_b32_e32 v2, v2, v9
	s_add_i32 s56, 0, 0x10000
	s_add_i32 s57, 0, 0x14000
	v_add_u32_e32 v186, s3, v170
	v_add_u32_e32 v187, s3, v174
	s_add_i32 s3, 0, 0x1c800
	v_mov_b32_e32 v139, v143
	v_mov_b32_e32 v141, v143
	v_or_b32_e32 v171, 16, v1
	v_or_b32_e32 v172, 32, v1
	v_or_b32_e32 v173, 48, v1
	v_lshl_add_u64 v[146:147], s[8:9], 0, v[142:143]
	v_mov_b32_e32 v149, v143
	v_lshl_add_u32 v150, v2, 1, v4
	v_mov_b32_e32 v151, v143
	v_mov_b64_e32 v[152:153], 0x300
	v_mov_b64_e32 v[154:155], 0x2ff
	v_add_u32_e32 v176, s56, v170
	v_add_u32_e32 v177, s56, v174
	v_add_u32_e32 v180, s57, v170
	v_add_u32_e32 v181, s57, v174
	v_add_u32_e32 v184, 0, v5
	v_add_u32_e32 v185, 0, v3
	v_add_u32_e32 v188, s3, v170
	v_add_u32_e32 v189, s3, v174
	s_mov_b64 s[24:25], 0xa0000
	s_mov_b32 s58, 0xa0000
	s_mov_b64 s[26:27], 0xb0000
	s_mov_b32 s59, 0xb0000
	s_mov_b32 s60, 0x6313600
	v_mov_b32_e32 v190, 0x3d800000
	s_mov_b32 s61, 0
	s_barrier
	s_branch .LBB0_1254

; __device__ __forceinline__ int tidx() { int t = threadIdx.x; asm volatile("" : "+v"(t)); return t; }
; __host__ __device__ __forceinline__ int lds_byte(int r, int c) { return (r >> 3) * 1024 + (r & 7) * 128 + ((((c >> 3) ^ r) & 7) << 4) + (c & 7) * 2; }
; #define PG8_STAGE(bufoff, gbase, voff) do { _Pragma("unroll") for (int _i = 0; _i < 2; ++_i) \
;         __builtin_amdgcn_global_load_lds((const unsigned*)((const char*)(gbase) + (voff)[_i]), (LAS unsigned*)(lds + (bufoff) + ldsw + _i * 8192), 16, 0, 0); } while (0)
; #define PG8_WAIT_V(n) asm volatile("s_waitcnt vmcnt(" #n ")" ::: "memory")
; #define PG8_BAR __builtin_amdgcn_s_barrier()
;     const int tid = tidx(), wid = __builtin_amdgcn_readfirstlane(tid >> 6), lane = tid & 63, wr = wid >> 2, wc = wid & 3, fr = lane & 15, fq = lane >> 4;
;     const int K = (int)g.K, ntf = K / BK;
;     int sR[2], sC[2]; unsigned voffB[2], voffA[2][2], voffN[2][2];
; #pragma unroll
;     for (int i = 0; i < 2; ++i) { stage_rc(tid * 16 + i * 8192, sR[i], sC[i]); const int Rb = Epi::PERM ? ((sR[i] & ~31) + perm32(sR[i] & 31)) : sR[i];
;         voffB[i] = (TILED & 2) ? (unsigned)(Rb * BK + sC[i]) * 2u : (unsigned)(Rb * K + sC[i]) * 2u; }
;     constexpr size_t kstepA = (TILED & 1) ? (size_t)HALF * BK * 2 : (size_t)(BK * 2), kstepB = (TILED & 2) ? (size_t)HALF * BK * 2 : (size_t)(BK * 2);
;     const size_t hstep = (size_t)HALF * K * 2;
;     const size_t tstep = 2 * hstep;
;     const unsigned ldsw = (unsigned)wid * 1024u;
;     const int aoff = lds_byte(wr * 64 + fr, fq * 8), boff = lds_byte(wc * 32 + fr, fq * 8);
;     ...
;     const char* cA = (const char*)(g.A + (size_t)cur.z * g.aStrideZ) + (GATHER ? (size_t)0 : (size_t)cur.pm * tstep) + k0t(cur) * kstepA;
;     const char* cB = (const char*)(g.Bt + (size_t)cur.z * g.bStrideZ) + (size_t)cur.pn * tstep + k0t(cur) * kstepB;
;     PG8_STAGE(PG8_SB(0, 0), cB, voffB); PG8_STAGE(PG8_SB(0, 1), cB + hstep, voffB); PG8_STAGE(PG8_SA(0, 0), cA, voffA[0]); PG8_STAGE(PG8_SA(0, 1), cA, voffA[1]);
;     if (wr == 1) PG8_BAR;
;     PG8_WAIT_V(2); PG8_BAR;
;     PG8_STAGE(PG8_SB(1, 0), cB + kstepB, voffB); PG8_STAGE(PG8_SA(1, 0), cA + kstepA, voffA[0]); PG8_STAGE(PG8_SB(1, 1), cB + hstep + kstepB, voffB);
;     PG8_WAIT_V(6); PG8_BAR;
.LBB0_1337:
	s_mov_b64 s[10:11], 0x80
	s_and_b32 s3, s6, 3
	s_add_i32 m0, s55, 0x18000
	v_lshl_add_u64 v[4:5], v[4:5], 0, s[10:11]
	s_lshl_b32 s42, s23, 6
	s_lshl_b32 s68, s3, 5
	global_load_lds_dwordx4 v[4:5], off
	s_add_i32 m0, s55, 0x1a000
	s_add_u32 s12, s56, 0x4000
	v_lshl_add_u64 v[2:3], v[2:3], 0, s[10:11]
	s_addc_u32 s13, s57, 0
	s_add_i32 s70, s55, 0x8000
	global_load_lds_dwordx4 v[2:3], off
	v_lshl_add_u64 v[2:3], s[12:13], 0, v[150:151]
	s_mov_b32 m0, s70
	s_add_i32 s71, s55, 0xa000
	global_load_lds_dwordx4 v[2:3], off
	v_lshl_add_u64 v[2:3], s[12:13], 0, v[152:153]
	s_add_u32 s12, s0, 0x40080
	s_mov_b32 m0, s71
	s_addc_u32 s13, s1, 0
	global_load_lds_dwordx4 v[2:3], off
	s_add_i32 m0, s55, 0x1c000
	v_lshl_add_u64 v[2:3], s[12:13], 0, v[146:147]
	global_load_lds_dwordx4 v[2:3], off
	v_lshl_add_u64 v[2:3], s[12:13], 0, v[148:149]
	s_add_i32 m0, s55, 0x1e000
	s_cmpk_lt_u32 s22, 0x100
	global_load_lds_dwordx4 v[2:3], off
	s_waitcnt vmcnt(8)
	s_barrier
	s_cselect_b64 s[12:13], -1, 0
	s_cmpk_gt_u32 s22, 0xff
	s_cselect_b64 s[24:25], -1, 0
	s_lshl_b32 s22, s23, 1
	s_lshl_b32 s44, s23, 13
	s_ashr_i32 s23, s22, 31
	s_lshl_b64 s[26:27], s[22:23], 13
	s_lshl_b64 s[28:29], s[22:23], 10
	s_add_i32 s23, s42, 0x80
	s_ashr_i32 s30, s23, 5
	s_add_i32 s23, s42, 0x90
	s_or_b32 s22, s22, 1
	v_lshlrev_b32_e32 v2, 1, v12
	s_ashr_i32 s34, s23, 5
	s_ashr_i32 s23, s22, 31
	v_and_b32_e32 v1, 15, v12
	v_bfe_u32 v15, v12, 4, 2
	v_and_b32_e32 v2, 32, v2
	s_lshl_b64 s[36:37], s[22:23], 13
	s_lshl_b64 s[38:39], s[22:23], 10
	s_add_i32 s22, s42, 0xa0
	v_lshlrev_b32_e32 v17, 3, v15
	v_or_b32_e32 v3, v2, v1
	s_ashr_i32 s22, s22, 5
	v_or_b32_e32 v16, s42, v1
	v_lshlrev_b32_e32 v160, 3, v3
	v_and_or_b32 v3, v17, 16, v1
	s_ashr_i32 s23, s22, 31
	s_addk_i32 s42, 0xb0
	v_lshlrev_b32_e32 v162, 3, v3
	v_lshlrev_b32_e32 v3, 5, v12
	v_or_b32_e32 v167, 16, v1
	s_lshl_b64 s[40:41], s[22:23], 10
	s_ashr_i32 s22, s42, 5
	s_lshl_b32 s3, s3, 11
	v_and_b32_e32 v3, 0x400, v3
	v_or_b32_e32 v2, v2, v167
	s_ashr_i32 s23, s22, 31
	v_lshlrev_b32_e32 v158, 10, v1
	s_lshl_b32 s6, s6, 8
	v_or_b32_e32 v164, s3, v3
	v_lshlrev_b32_e32 v166, 3, v2
	s_lshl_b64 s[42:43], s[22:23], 10
	v_lshl_add_u64 v[2:3], s[48:49], 0, v[158:159]
	s_and_b32 s6, s6, 0x100
	s_add_i32 s22, s44, 0
	v_lshl_add_u64 v[2:3], v[2:3], 0, s[6:7]
	v_lshlrev_b32_e32 v158, 6, v15
	s_add_i32 s3, s22, s3
	v_and_b32_e32 v4, 16, v12
	v_and_b32_e32 v5, 0x200, v13
	v_lshl_add_u64 v[168:169], v[2:3], 0, v[158:159]
	s_add_i32 s3, s3, 0x20000
	v_lshlrev_b32_e32 v2, 6, v1
	v_lshlrev_b32_e32 v3, 4, v15
	v_add3_u32 v189, s3, v2, v3
	v_add_u32_e32 v2, s3, v5
	v_lshlrev_b32_e32 v3, 1, v1
	v_lshlrev_b32_e32 v5, 1, v4
	v_add3_u32 v190, v2, v3, v5
	v_lshlrev_b32_e32 v2, 10, v167
	v_mov_b32_e32 v3, v159
	v_lshl_add_u64 v[2:3], s[48:49], 0, v[2:3]
	v_or_b32_e32 v186, 32, v1
	v_lshl_add_u64 v[2:3], v[2:3], 0, s[6:7]
	v_lshl_add_u64 v[170:171], v[2:3], 0, v[158:159]
	v_lshlrev_b32_e32 v2, 10, v186
	v_mov_b32_e32 v3, v159
	v_lshl_add_u64 v[2:3], s[48:49], 0, v[2:3]
	v_or_b32_e32 v187, 48, v1
	v_lshl_add_u64 v[2:3], v[2:3], 0, s[6:7]
	v_lshl_add_u64 v[172:173], v[2:3], 0, v[158:159]
	v_lshlrev_b32_e32 v2, 10, v187
	v_mov_b32_e32 v3, v159
	v_writelane_b32 v250, s48, 39
	v_lshrrev_b32_e32 v14, 4, v12
	v_and_b32_e32 v19, 7, v12
	v_lshl_add_u64 v[2:3], s[48:49], 0, v[2:3]
	v_lshl_add_u64 v[2:3], v[2:3], 0, s[6:7]
	v_lshl_add_u64 v[174:175], v[2:3], 0, v[158:159]
	v_lshlrev_b32_e32 v2, 7, v7
	v_lshl_add_u32 v2, v6, 10, v2
	v_or_b32_e32 v2, v2, v8
	v_bitop3_b32 v14, v14, v19, 3 bitop3:0x6c
	v_add_u32_e32 v176, 0x40000, v2
	v_lshlrev_b32_e32 v2, 7, v10
	v_lshlrev_b32_e32 v18, 7, v16
	v_lshlrev_b32_e32 v14, 4, v14
	v_or_b32_e32 v20, s68, v1
	s_waitcnt vmcnt(6)
	v_lshl_add_u32 v2, v9, 10, v2
	v_or_b32_e32 v19, v18, v14
	v_lshlrev_b32_e32 v20, 7, v20
	s_ashr_i32 s31, s30, 31
	s_ashr_i32 s35, s34, 31
	v_bitop3_b32 v12, v18, 64, v14 bitop3:0x36
	v_or_b32_e32 v2, v2, v11
	v_mov_b32_e32 v155, v159
	v_mov_b32_e32 v157, v159
	v_or_b32_e32 v161, v20, v14
	s_mov_b32 s69, 0x8000
	v_add_u32_e32 v163, 0xfffff800, v16
	v_mov_b32_e32 v165, v159
	s_lshl_b64 s[30:31], s[30:31], 10
	s_lshl_b64 s[34:35], s[34:35], 10
	v_bitop3_b32 v188, v20, 64, v14 bitop3:0x36
	v_or_b32_e32 v191, s68, v17
	v_or_b32_e32 v192, s68, v4
	v_mov_b32_e32 v177, v159
	v_add_u32_e32 v178, 0x40000, v2
	v_mov_b32_e32 v179, v159
	s_add_i32 s92, 0, 0x10000
	s_add_i32 s93, 0, 0x10800
	s_add_i32 s62, 0, 0x14000
	s_add_i32 s63, 0, 0x14800
	v_add_u32_e32 v193, 0, v19
	v_add_u32_e32 v194, 0, v12
	s_add_i32 s72, 0, 0x18800
	s_add_i32 s73, 0, 0x1c800
	s_mov_b32 s22, 0x8400
	s_mov_b32 s6, 0x3d800000
	s_barrier
	v_writelane_b32 v250, s49, 40
	s_branch .LBB0_1340

; __device__ __forceinline__ int tidx() { int t = threadIdx.x; asm volatile("" : "+v"(t)); return t; }
; __host__ __device__ __forceinline__ int lds_byte(int r, int c) { return (r >> 3) * 1024 + (r & 7) * 128 + ((((c >> 3) ^ r) & 7) << 4) + (c & 7) * 2; }
; #define PG8_STAGE(bufoff, gbase, voff) do { _Pragma("unroll") for (int _i = 0; _i < 2; ++_i) \
;         __builtin_amdgcn_global_load_lds((const unsigned*)((const char*)(gbase) + (voff)[_i]), (LAS unsigned*)(lds + (bufoff) + ldsw + _i * 8192), 16, 0, 0); } while (0)
; #define PG8_WAIT_V(n) asm volatile("s_waitcnt vmcnt(" #n ")" ::: "memory")
; #define PG8_BAR __builtin_amdgcn_s_barrier()
;     const int tid = tidx(), wid = __builtin_amdgcn_readfirstlane(tid >> 6), lane = tid & 63, wr = wid >> 2, wc = wid & 3, fr = lane & 15, fq = lane >> 4;
;     const int K = (int)g.K, ntf = K / BK;
;     int sR[2], sC[2]; unsigned voffB[2], voffA[2][2], voffN[2][2];
; #pragma unroll
;     for (int i = 0; i < 2; ++i) { stage_rc(tid * 16 + i * 8192, sR[i], sC[i]); const int Rb = Epi::PERM ? ((sR[i] & ~31) + perm32(sR[i] & 31)) : sR[i];
;         voffB[i] = (TILED & 2) ? (unsigned)(Rb * BK + sC[i]) * 2u : (unsigned)(Rb * K + sC[i]) * 2u; }
;     constexpr size_t kstepA = (TILED & 1) ? (size_t)HALF * BK * 2 : (size_t)(BK * 2), kstepB = (TILED & 2) ? (size_t)HALF * BK * 2 : (size_t)(BK * 2);
;     const size_t hstep = (size_t)HALF * K * 2;
;     const size_t tstep = 2 * hstep;
;     const unsigned ldsw = (unsigned)wid * 1024u;
;     const int aoff = lds_byte(wr * 64 + fr, fq * 8), boff = lds_byte(wc * 32 + fr, fq * 8);
;     ...
;     const char* cA = (const char*)(g.A + (size_t)cur.z * g.aStrideZ) + (GATHER ? (size_t)0 : (size_t)cur.pm * tstep) + k0t(cur) * kstepA;
;     const char* cB = (const char*)(g.Bt + (size_t)cur.z * g.bStrideZ) + (size_t)cur.pn * tstep + k0t(cur) * kstepB;
;     PG8_STAGE(PG8_SB(0, 0), cB, voffB); PG8_STAGE(PG8_SB(0, 1), cB + hstep, voffB); PG8_STAGE(PG8_SA(0, 0), cA, voffA[0]); PG8_STAGE(PG8_SA(0, 1), cA, voffA[1]);
;     if (wr == 1) PG8_BAR;
;     PG8_WAIT_V(2); PG8_BAR;
;     PG8_STAGE(PG8_SB(1, 0), cB + kstepB, voffB); PG8_STAGE(PG8_SA(1, 0), cA + kstepA, voffA[0]); PG8_STAGE(PG8_SB(1, 1), cB + hstep + kstepB, voffB);
;     PG8_WAIT_V(6); PG8_BAR;
.LBB0_1492:
	s_mov_b64 s[24:25], 0x80
	s_and_b32 s3, s10, 3
	s_add_i32 m0, s61, 0x18000
	v_lshl_add_u64 v[4:5], v[4:5], 0, s[24:25]
	s_lshl_b32 s9, s13, 6
	s_lshl_b32 s67, s3, 5
	global_load_lds_dwordx4 v[4:5], off
	s_add_i32 m0, s61, 0x1a000
	s_add_u32 s22, s6, 0x4000
	v_lshl_add_u64 v[2:3], v[2:3], 0, s[24:25]
	s_addc_u32 s23, s7, 0
	s_add_i32 s68, s61, 0x8000
	global_load_lds_dwordx4 v[2:3], off
	v_lshl_add_u64 v[2:3], s[22:23], 0, v[142:143]
	s_mov_b32 m0, s68
	s_add_i32 s69, s61, 0xa000
	global_load_lds_dwordx4 v[2:3], off
	v_lshl_add_u64 v[2:3], s[22:23], 0, v[144:145]
	s_add_u32 s22, s0, 0x40080
	s_mov_b32 m0, s69
	s_addc_u32 s23, s1, 0
	global_load_lds_dwordx4 v[2:3], off
	s_add_i32 m0, s61, 0x1c000
	v_lshl_add_u64 v[2:3], s[22:23], 0, v[138:139]
	global_load_lds_dwordx4 v[2:3], off
	v_lshl_add_u64 v[2:3], s[22:23], 0, v[140:141]
	s_add_i32 m0, s61, 0x1e000
	s_cmpk_lt_u32 s12, 0x100
	global_load_lds_dwordx4 v[2:3], off
	s_waitcnt vmcnt(8)
	s_barrier
	s_cselect_b64 s[26:27], -1, 0
	s_cmpk_gt_u32 s12, 0xff
	s_cselect_b64 s[28:29], -1, 0
	s_lshl_b32 s12, s13, 1
	s_lshl_b32 s18, s13, 13
	s_ashr_i32 s13, s12, 31
	s_lshl_b64 s[30:31], s[12:13], 13
	s_lshl_b64 s[34:35], s[12:13], 10
	s_add_i32 s13, s9, 0x80
	s_ashr_i32 s22, s13, 5
	s_ashr_i32 s23, s22, 31
	s_lshl_b64 s[22:23], s[22:23], 10
	v_lshlrev_b32_e32 v2, 1, v12
	v_writelane_b32 v250, s22, 39
	s_add_i32 s13, s9, 0x90
	s_or_b32 s12, s12, 1
	v_and_b32_e32 v1, 15, v12
	v_bfe_u32 v15, v12, 4, 2
	v_and_b32_e32 v2, 32, v2
	v_writelane_b32 v250, s23, 40
	s_ashr_i32 s22, s13, 5
	s_ashr_i32 s13, s12, 31
	v_lshlrev_b32_e32 v17, 3, v15
	v_or_b32_e32 v3, v2, v1
	s_lshl_b64 s[40:41], s[12:13], 13
	s_lshl_b64 s[42:43], s[12:13], 10
	s_add_i32 s12, s9, 0xa0
	v_lshlrev_b32_e32 v152, 3, v3
	v_and_or_b32 v3, v17, 16, v1
	s_ashr_i32 s12, s12, 5
	v_or_b32_e32 v16, s9, v1
	v_lshlrev_b32_e32 v154, 3, v3
	v_lshlrev_b32_e32 v3, 5, v12
	v_or_b32_e32 v159, 16, v1
	s_ashr_i32 s13, s12, 31
	s_addk_i32 s9, 0xb0
	s_lshl_b32 s3, s3, 11
	v_and_b32_e32 v3, 0x400, v3
	v_or_b32_e32 v2, v2, v159
	s_lshl_b64 s[44:45], s[12:13], 10
	s_ashr_i32 s12, s9, 5
	v_lshlrev_b32_e32 v150, 10, v1
	s_lshl_b32 s9, s10, 8
	v_or_b32_e32 v156, s3, v3
	v_lshlrev_b32_e32 v158, 3, v2
	v_lshl_add_u64 v[2:3], s[48:49], 0, v[150:151]
	s_and_b32 s10, s9, 0x100
	s_add_i32 s9, s18, 0
	v_lshl_add_u64 v[2:3], v[2:3], 0, s[10:11]
	v_lshlrev_b32_e32 v150, 6, v15
	s_add_i32 s3, s9, s3
	v_and_b32_e32 v4, 16, v12
	v_and_b32_e32 v5, 0x200, v13
	v_lshl_add_u64 v[160:161], v[2:3], 0, v[150:151]
	s_add_i32 s3, s3, 0x20000
	v_lshlrev_b32_e32 v2, 6, v1
	v_lshlrev_b32_e32 v3, 4, v15
	v_add3_u32 v185, s3, v2, v3
	v_add_u32_e32 v2, s3, v5
	v_lshlrev_b32_e32 v3, 1, v1
	v_lshlrev_b32_e32 v5, 1, v4
	v_add3_u32 v186, v2, v3, v5
	v_lshlrev_b32_e32 v2, 10, v159
	v_mov_b32_e32 v3, v151
	v_lshl_add_u64 v[2:3], s[48:49], 0, v[2:3]
	v_or_b32_e32 v182, 32, v1
	v_lshl_add_u64 v[2:3], v[2:3], 0, s[10:11]
	v_lshl_add_u64 v[162:163], v[2:3], 0, v[150:151]
	v_lshlrev_b32_e32 v2, 10, v182
	v_mov_b32_e32 v3, v151
	v_lshl_add_u64 v[2:3], s[48:49], 0, v[2:3]
	v_or_b32_e32 v183, 48, v1
	v_lshl_add_u64 v[2:3], v[2:3], 0, s[10:11]
	v_lshl_add_u64 v[164:165], v[2:3], 0, v[150:151]
	v_lshlrev_b32_e32 v2, 10, v183
	v_mov_b32_e32 v3, v151
	v_lshl_add_u64 v[2:3], s[48:49], 0, v[2:3]
	v_lshl_add_u64 v[2:3], v[2:3], 0, s[10:11]
	v_lshl_add_u64 v[166:167], v[2:3], 0, v[150:151]
	v_lshlrev_b32_e32 v2, 7, v7
	v_lshl_add_u32 v2, v6, 10, v2
	v_lshrrev_b32_e32 v14, 4, v12
	v_and_b32_e32 v19, 7, v12
	v_or_b32_e32 v2, v2, v8
	v_bitop3_b32 v14, v14, v19, 3 bitop3:0x6c
	v_add_u32_e32 v168, 0x40000, v2
	v_lshlrev_b32_e32 v2, 7, v10
	v_lshlrev_b32_e32 v18, 7, v16
	v_lshlrev_b32_e32 v14, 4, v14
	v_or_b32_e32 v20, s67, v1
	s_waitcnt vmcnt(6)
	v_lshl_add_u32 v2, v9, 10, v2
	v_or_b32_e32 v19, v18, v14
	v_lshlrev_b32_e32 v20, 7, v20
	s_ashr_i32 s23, s22, 31
	s_ashr_i32 s13, s12, 31
	v_bitop3_b32 v12, v18, 64, v14 bitop3:0x36
	v_or_b32_e32 v2, v2, v11
	v_mov_b32_e32 v147, v151
	v_mov_b32_e32 v149, v151
	v_or_b32_e32 v153, v20, v14
	v_add_u32_e32 v155, 0xfffff800, v16
	v_mov_b32_e32 v157, v151
	s_lshl_b64 s[38:39], s[22:23], 10
	s_lshl_b64 s[46:47], s[12:13], 10
	v_bitop3_b32 v184, v20, 64, v14 bitop3:0x36
	v_or_b32_e32 v187, s67, v17
	v_or_b32_e32 v188, s67, v4
	v_mov_b32_e32 v169, v151
	v_add_u32_e32 v170, 0x40000, v2
	v_mov_b32_e32 v171, v151
	s_add_i32 s70, 0, 0x10000
	s_add_i32 s71, 0, 0x10800
	s_add_i32 s92, 0, 0x14000
	s_add_i32 s93, 0, 0x14800
	v_add_u32_e32 v189, 0, v19
	v_add_u32_e32 v190, 0, v12
	s_add_i32 s12, 0, 0x18800
	s_add_i32 s13, 0, 0x1c800
	s_mov_b32 s36, 0x8400
	s_mov_b32 s10, 0x3d800000
	s_barrier
	s_branch .LBB0_1495

; __device__ __forceinline__ int tidx() { int t = threadIdx.x; asm volatile("" : "+v"(t)); return t; }
; __host__ __device__ __forceinline__ int lds_byte(int r, int c) { return (r >> 3) * 1024 + (r & 7) * 128 + ((((c >> 3) ^ r) & 7) << 4) + (c & 7) * 2; }
; #define PG8_STAGE(bufoff, gbase, voff) do { _Pragma("unroll") for (int _i = 0; _i < 2; ++_i) \
;         __builtin_amdgcn_global_load_lds((const unsigned*)((const char*)(gbase) + (voff)[_i]), (LAS unsigned*)(lds + (bufoff) + ldsw + _i * 8192), 16, 0, 0); } while (0)
; #define PG8_WAIT_V(n) asm volatile("s_waitcnt vmcnt(" #n ")" ::: "memory")
;     const int tid = tidx(), wid = __builtin_amdgcn_readfirstlane(tid >> 6), lane = tid & 63, wr = wid >> 2, wc = wid & 3, fr = lane & 15, fq = lane >> 4;
;     const int K = (int)g.K, ntf = K / BK;
;     int sR[2], sC[2]; unsigned voffB[2], voffA[2][2], voffN[2][2];
; #pragma unroll
;     for (int i = 0; i < 2; ++i) { stage_rc(tid * 16 + i * 8192, sR[i], sC[i]); const int Rb = Epi::PERM ? ((sR[i] & ~31) + perm32(sR[i] & 31)) : sR[i];
;         voffB[i] = (TILED & 2) ? (unsigned)(Rb * BK + sC[i]) * 2u : (unsigned)(Rb * K + sC[i]) * 2u; }
;     constexpr size_t kstepA = (TILED & 1) ? (size_t)HALF * BK * 2 : (size_t)(BK * 2), kstepB = (TILED & 2) ? (size_t)HALF * BK * 2 : (size_t)(BK * 2);
;     const size_t hstep = (size_t)HALF * K * 2;
;     const size_t tstep = 2 * hstep;
;     const unsigned ldsw = (unsigned)wid * 1024u;
;     const int aoff = lds_byte(wr * 64 + fr, fq * 8), boff = lds_byte(wc * 32 + fr, fq * 8);
;     ...
;     const char* cA = (const char*)(g.A + (size_t)cur.z * g.aStrideZ) + (GATHER ? (size_t)0 : (size_t)cur.pm * tstep) + k0t(cur) * kstepA;
;     const char* cB = (const char*)(g.Bt + (size_t)cur.z * g.bStrideZ) + (size_t)cur.pn * tstep + k0t(cur) * kstepB;
;     PG8_STAGE(PG8_SB(0, 0), cB, voffB); PG8_STAGE(PG8_SB(0, 1), cB + hstep, voffB); PG8_STAGE(PG8_SA(0, 0), cA, voffA[0]); PG8_STAGE(PG8_SA(0, 1), cA, voffA[1]);
;     if (wr == 1) PG8_BAR;
;     PG8_WAIT_V(2); PG8_BAR;
;     PG8_STAGE(PG8_SB(1, 0), cB + kstepB, voffB); PG8_STAGE(PG8_SA(1, 0), cA + kstepA, voffA[0]); PG8_STAGE(PG8_SB(1, 1), cB + hstep + kstepB, voffB);
;     PG8_WAIT_V(6); PG8_BAR;
;     ...
;         const bool shortu = cur.pm >= SHORT_PM, do0 = (HALFM && cur.kq >= 0) ? cur.kq == 0 : (!shortu || wr == 0), do1 = (HALFM && cur.kq >= 0) ? cur.kq == 1 : !shortu;
.LBB0_1657:
	s_and_b32 s9, s1, 3
	s_lshl_b32 s42, s29, 6
	s_lshl_b32 s43, s9, 5
	s_and_b32 s1, s94, 1
	s_add_i32 s44, s31, 0x18000
	s_mov_b64 s[14:15], 0x80
	s_add_i32 s45, s31, 0x1a000
	v_lshl_add_u64 v[4:5], v[4:5], 0, s[14:15]
	s_mov_b32 m0, s44
	s_add_u32 s2, s12, 0x4000
	global_load_lds_dwordx4 v[4:5], off
	v_lshl_add_u64 v[2:3], v[2:3], 0, s[14:15]
	s_mov_b32 m0, s45
	s_addc_u32 s3, s13, 0
	s_add_i32 s46, s31, 0x8000
	global_load_lds_dwordx4 v[2:3], off
	v_lshl_add_u64 v[2:3], s[2:3], 0, v[200:201]
	s_mov_b32 m0, s46
	s_add_i32 s47, s31, 0xa000
	global_load_lds_dwordx4 v[2:3], off
	v_lshl_add_u64 v[2:3], s[2:3], 0, v[202:203]
	s_add_u32 s2, s10, 0x40080
	s_mov_b32 m0, s47
	s_addc_u32 s3, s11, 0
	s_add_i32 s48, s31, 0x1c000
	global_load_lds_dwordx4 v[2:3], off
	v_lshl_add_u64 v[2:3], s[2:3], 0, v[196:197]
	s_mov_b32 m0, s48
	s_add_i32 s49, s31, 0x1e000
	global_load_lds_dwordx4 v[2:3], off
	v_lshl_add_u64 v[2:3], s[2:3], 0, v[194:195]
	s_mov_b32 m0, s49
	s_cmp_eq_u32 s1, 0
	global_load_lds_dwordx4 v[2:3], off
	s_waitcnt vmcnt(8)
	s_barrier
	s_cselect_b64 s[6:7], -1, 0
	s_cmp_eq_u32 s1, 1
	s_cselect_b64 s[2:3], -1, 0
	s_lshl_b32 s1, s94, 18
	v_lshlrev_b32_e32 v2, 7, v9
	s_and_b32 s1, s1, 0x80000
	v_lshl_add_u32 v2, v10, 10, v2
	s_or_b32 s50, s1, 0x6213700
	s_ashr_i32 s1, s0, 31
	v_or_b32_e32 v2, v2, v11
	s_lshl_b64 s[0:1], s[0:1], 19
	v_add_u32_e32 v2, 0x40000, v2
	v_mov_b32_e32 v3, v197
	v_lshl_add_u64 v[2:3], s[0:1], 0, v[2:3]
	s_mov_b64 s[22:23], 0x2fc17600
	v_lshl_add_u64 v[208:209], v[2:3], 0, s[22:23]
	v_lshlrev_b32_e32 v2, 7, v7
	v_lshrrev_b32_e32 v13, 4, v12
	v_and_b32_e32 v1, 15, v12
	v_bfe_u32 v199, v12, 4, 2
	v_and_b32_e32 v12, 7, v12
	v_lshl_add_u32 v2, v6, 10, v2
	v_bitop3_b32 v12, v13, v12, 3 bitop3:0x6c
	v_or_b32_e32 v15, s43, v1
	v_or_b32_e32 v2, v2, v8
	v_lshlrev_b32_e32 v12, 4, v12
	v_lshlrev_b32_e32 v15, 7, v15
	s_add_u32 s51, s0, 0x2fc1b600
	v_add_u32_e32 v2, 0x40000, v2
	v_mov_b32_e32 v3, v197
	v_or_b32_e32 v216, v15, v12
	v_bitop3_b32 v217, v15, 64, v12 bitop3:0x36
	s_addc_u32 s52, s1, 0
	v_lshl_add_u64 v[2:3], s[0:1], 0, v[2:3]
	s_add_i32 s0, 0, 0x10000
	v_or_b32_e32 v14, s42, v1
	v_add_u32_e32 v218, s0, v216
	v_add_u32_e32 v219, s0, v217
	s_add_i32 s0, 0, 0x10800
	v_lshlrev_b32_e32 v14, 7, v14
	v_add_u32_e32 v220, s0, v216
	v_add_u32_e32 v221, s0, v217
	s_add_i32 s0, 0, 0x14000
	v_or_b32_e32 v13, v14, v12
	s_waitcnt vmcnt(6)
	v_bitop3_b32 v12, v14, 64, v12 bitop3:0x36
	v_mov_b32_e32 v4, v197
	v_mov_b32_e32 v5, v197
	v_add_u32_e32 v222, s0, v216
	v_add_u32_e32 v223, s0, v217
	s_add_i32 s0, 0, 0x14800
	v_cndmask_b32_e64 v6, 0, 1, s[6:7]
	v_lshl_add_u64 v[210:211], v[2:3], 0, s[22:23]
	v_mov_b32_e32 v2, v197
	v_mov_b32_e32 v3, v197
	v_add_u32_e32 v224, s0, v216
	v_add_u32_e32 v225, s0, v217
	v_add_u32_e32 v226, 0, v13
	v_add_u32_e32 v227, 0, v12
	v_cmp_ne_u32_e64 s[0:1], 1, v6
	v_mov_b64_e32 v[16:17], v[4:5]
	v_mov_b64_e32 v[44:45], v[4:5]
	v_mov_b64_e32 v[48:49], v[4:5]
	v_mov_b64_e32 v[76:77], v[4:5]
	v_mov_b64_e32 v[80:81], v[4:5]
	v_mov_b64_e32 v[108:109], v[4:5]
	v_mov_b64_e32 v[112:113], v[4:5]
	v_mov_b64_e32 v[28:29], v[4:5]
	v_mov_b64_e32 v[32:33], v[4:5]
	v_mov_b64_e32 v[60:61], v[4:5]
	v_mov_b64_e32 v[64:65], v[4:5]
	v_mov_b64_e32 v[92:93], v[4:5]
	v_mov_b64_e32 v[96:97], v[4:5]
	v_mov_b64_e32 v[124:125], v[4:5]
	v_mov_b64_e32 v[128:129], v[4:5]
	v_mov_b64_e32 v[12:13], v[4:5]
	v_mov_b64_e32 v[8:9], v[4:5]
	v_mov_b64_e32 v[40:41], v[4:5]
	v_mov_b64_e32 v[36:37], v[4:5]
	v_mov_b64_e32 v[72:73], v[4:5]
	v_mov_b64_e32 v[68:69], v[4:5]
	v_mov_b64_e32 v[104:105], v[4:5]
	v_mov_b64_e32 v[100:101], v[4:5]
	v_mov_b64_e32 v[24:25], v[4:5]
	v_mov_b64_e32 v[20:21], v[4:5]
	v_mov_b64_e32 v[56:57], v[4:5]
	v_mov_b64_e32 v[52:53], v[4:5]
	v_mov_b64_e32 v[88:89], v[4:5]
	v_mov_b64_e32 v[84:85], v[4:5]
	v_mov_b64_e32 v[120:121], v[4:5]
	v_mov_b64_e32 v[116:117], v[4:5]
	v_mov_b32_e32 v205, v197
	v_mov_b32_e32 v207, v197
	s_mov_b32 s53, -2
	s_add_i32 s54, s31, 0xc000
	s_add_i32 s55, s31, 0xe000
	s_add_i32 s56, 0, 0x18800
	s_add_i32 s57, 0, 0x1c800
	s_mov_b64 s[22:23], 0x8000
	s_add_i32 s58, 0, 0x18000
	s_add_i32 s59, 0, 0x1c000
	v_mov_b64_e32 v[14:15], v[2:3]
	v_mov_b64_e32 v[42:43], v[2:3]
	v_mov_b64_e32 v[46:47], v[2:3]
	v_mov_b64_e32 v[74:75], v[2:3]
	v_mov_b64_e32 v[78:79], v[2:3]
	v_mov_b64_e32 v[106:107], v[2:3]
	v_mov_b64_e32 v[110:111], v[2:3]
	v_mov_b64_e32 v[26:27], v[2:3]
	v_mov_b64_e32 v[30:31], v[2:3]
	v_mov_b64_e32 v[58:59], v[2:3]
	v_mov_b64_e32 v[62:63], v[2:3]
	v_mov_b64_e32 v[90:91], v[2:3]
	v_mov_b64_e32 v[94:95], v[2:3]
	v_mov_b64_e32 v[122:123], v[2:3]
	v_mov_b64_e32 v[126:127], v[2:3]
	v_mov_b64_e32 v[10:11], v[2:3]
	v_mov_b64_e32 v[6:7], v[2:3]
	v_mov_b64_e32 v[38:39], v[2:3]
	v_mov_b64_e32 v[34:35], v[2:3]
	v_mov_b64_e32 v[70:71], v[2:3]
	v_mov_b64_e32 v[66:67], v[2:3]
	v_mov_b64_e32 v[102:103], v[2:3]
	v_mov_b64_e32 v[98:99], v[2:3]
	v_mov_b64_e32 v[22:23], v[2:3]
	v_mov_b64_e32 v[18:19], v[2:3]
	v_mov_b64_e32 v[54:55], v[2:3]
	v_mov_b64_e32 v[50:51], v[2:3]
	v_mov_b64_e32 v[86:87], v[2:3]
	v_mov_b64_e32 v[82:83], v[2:3]
	v_mov_b64_e32 v[118:119], v[2:3]
	v_mov_b64_e32 v[114:115], v[2:3]
	s_barrier
	s_branch .LBB0_1659

; __device__ __forceinline__ int tidx() { int t = threadIdx.x; asm volatile("" : "+v"(t)); return t; }
; __host__ __device__ __forceinline__ int lds_byte(int r, int c) { return (r >> 3) * 1024 + (r & 7) * 128 + ((((c >> 3) ^ r) & 7) << 4) + (c & 7) * 2; }
; #define PG8_STAGE(bufoff, gbase, voff) do { _Pragma("unroll") for (int _i = 0; _i < 2; ++_i) \
;         __builtin_amdgcn_global_load_lds((const unsigned*)((const char*)(gbase) + (voff)[_i]), (LAS unsigned*)(lds + (bufoff) + ldsw + _i * 8192), 16, 0, 0); } while (0)
; #define PG8_WAIT_V(n) asm volatile("s_waitcnt vmcnt(" #n ")" ::: "memory")
; #define PG8_BAR __builtin_amdgcn_s_barrier()
;     const int tid = tidx(), wid = __builtin_amdgcn_readfirstlane(tid >> 6), lane = tid & 63, wr = wid >> 2, wc = wid & 3, fr = lane & 15, fq = lane >> 4;
;     const int K = (int)g.K, ntf = K / BK;
;     int sR[2], sC[2]; unsigned voffB[2], voffA[2][2], voffN[2][2];
; #pragma unroll
;     for (int i = 0; i < 2; ++i) { stage_rc(tid * 16 + i * 8192, sR[i], sC[i]); const int Rb = Epi::PERM ? ((sR[i] & ~31) + perm32(sR[i] & 31)) : sR[i];
;         voffB[i] = (TILED & 2) ? (unsigned)(Rb * BK + sC[i]) * 2u : (unsigned)(Rb * K + sC[i]) * 2u; }
;     constexpr size_t kstepA = (TILED & 1) ? (size_t)HALF * BK * 2 : (size_t)(BK * 2), kstepB = (TILED & 2) ? (size_t)HALF * BK * 2 : (size_t)(BK * 2);
;     const size_t hstep = (size_t)HALF * K * 2;
;     const size_t tstep = 2 * hstep;
;     const unsigned ldsw = (unsigned)wid * 1024u;
;     const int aoff = lds_byte(wr * 64 + fr, fq * 8), boff = lds_byte(wc * 32 + fr, fq * 8);
;     ...
;     const char* cA = (const char*)(g.A + (size_t)cur.z * g.aStrideZ) + (GATHER ? (size_t)0 : (size_t)cur.pm * tstep) + k0t(cur) * kstepA;
;     const char* cB = (const char*)(g.Bt + (size_t)cur.z * g.bStrideZ) + (size_t)cur.pn * tstep + k0t(cur) * kstepB;
;     PG8_STAGE(PG8_SB(0, 0), cB, voffB); PG8_STAGE(PG8_SB(0, 1), cB + hstep, voffB); PG8_STAGE(PG8_SA(0, 0), cA, voffA[0]); PG8_STAGE(PG8_SA(0, 1), cA, voffA[1]);
;     if (wr == 1) PG8_BAR;
;     PG8_WAIT_V(2); PG8_BAR;
;     PG8_STAGE(PG8_SB(1, 0), cB + kstepB, voffB); PG8_STAGE(PG8_SA(1, 0), cA + kstepA, voffA[0]); PG8_STAGE(PG8_SB(1, 1), cB + hstep + kstepB, voffB);
;     PG8_WAIT_V(6); PG8_BAR;
.LBB0_1924:
	v_readlane_b32 s12, v250, 10
	v_readlane_b32 s14, v250, 12
	v_readlane_b32 s15, v250, 13
	v_readlane_b32 s26, v250, 24
	v_readlane_b32 s27, v250, 25
	s_mov_b64 s[14:15], s[26:27]
	v_readlane_b32 s13, v250, 11
	s_add_u32 s12, s14, 0x1000
	s_addc_u32 s13, s15, 0
	s_add_u32 s14, s78, 0x10000
	v_readlane_b32 s16, v250, 14
	s_addc_u32 s15, s79, 0
	s_and_b32 s56, s3, 3
	v_readlane_b32 s17, v250, 15
	s_add_u32 s16, s0, 0x4000
	s_addc_u32 s17, s1, 0
	s_add_i32 m0, s52, 0x18000
	v_lshl_add_u64 v[12:13], s[16:17], 0, v[146:147]
	v_readlane_b32 s18, v250, 16
	global_load_lds_dwordx4 v[12:13], off
	v_lshl_add_u64 v[12:13], s[16:17], 0, v[148:149]
	s_add_i32 m0, s52, 0x1a000
	s_mov_b64 s[16:17], 0x80
	s_add_i32 s57, s52, 0x8000
	s_add_i32 s58, s52, 0xa000
	v_readlane_b32 s19, v250, 17
	global_load_lds_dwordx4 v[12:13], off
	v_lshl_add_u64 v[2:3], v[2:3], 0, s[16:17]
	s_mov_b32 m0, s57
	s_add_u32 s18, s0, 0x84000
	global_load_lds_dwordx4 v[2:3], off
	v_lshl_add_u64 v[2:3], v[4:5], 0, s[16:17]
	s_mov_b32 m0, s58
	s_addc_u32 s19, s1, 0
	global_load_lds_dwordx4 v[2:3], off
	s_add_i32 m0, s52, 0x1c000
	v_lshl_add_u64 v[2:3], s[18:19], 0, v[146:147]
	global_load_lds_dwordx4 v[2:3], off
	v_lshl_add_u64 v[2:3], s[18:19], 0, v[148:149]
	s_add_i32 m0, s52, 0x1e000
	s_cmpk_lt_u32 s2, 0x100
	global_load_lds_dwordx4 v[2:3], off
	s_waitcnt vmcnt(8)
	s_barrier
	v_readlane_b32 s20, v250, 18
	s_cselect_b64 s[18:19], -1, 0
	s_ashr_i32 s59, s33, 31
	s_ashr_i32 s60, s94, 31
	v_readlane_b32 s21, v250, 19
	s_add_u32 s20, s90, 0x13600
	s_addc_u32 s21, s91, 0
	s_add_u32 s61, s90, 0x51a27600
	s_addc_u32 s62, s91, 0
	s_add_u32 s63, s90, 0x12a13600
	s_addc_u32 s64, s91, 0
	v_lshrrev_b32_e32 v2, 4, v1
	v_and_b32_e32 v187, 15, v1
	v_and_b32_e32 v5, 7, v1
	s_add_u32 s65, s90, 0xb600
	v_readlane_b32 s22, v250, 20
	v_lshlrev_b32_e32 v3, 7, v187
	v_bitop3_b32 v2, v2, v5, 3 bitop3:0x6c
	s_addc_u32 s66, s91, 0
	v_readlane_b32 s23, v250, 21
	v_lshl_or_b32 v4, s50, 13, v3
	v_lshlrev_b32_e32 v2, 4, v2
	v_lshl_or_b32 v3, s56, 12, v3
	s_add_u32 s22, s90, 0x51a37600
	v_readlane_b32 s24, v250, 22
	v_or_b32_e32 v189, v3, v2
	v_bitop3_b32 v190, v3, 64, v2 bitop3:0x36
	s_addc_u32 s23, s91, 0
	v_lshlrev_b32_e32 v3, 11, v10
	v_readlane_b32 s25, v250, 23
	s_add_u32 s24, s90, 0x51b37600
	v_lshl_add_u32 v3, v9, 14, v3
	v_or_b32_e32 v5, v2, v4
	v_bitop3_b32 v2, v2, 64, v4 bitop3:0x36
	s_addc_u32 s25, s91, 0
	v_or_b32_e32 v3, v3, v11
	v_mov_b32_e32 v4, 0x80000
	s_add_i32 s2, 0, 0x10800
	v_lshl_add_u32 v160, v3, 1, v4
	v_lshlrev_b32_e32 v3, 11, v7
	v_add_u32_e32 v193, s2, v189
	v_add_u32_e32 v194, s2, v190
	s_add_i32 s2, 0, 0x14800
	s_waitcnt vmcnt(6)
	v_lshl_add_u32 v3, v6, 14, v3
	v_add_u32_e32 v197, s2, v189
	v_add_u32_e32 v199, s2, v190
	s_add_i32 s2, 0, 0x18800
	v_or_b32_e32 v3, v3, v8
	s_add_i32 s67, 0, 0x10000
	s_add_i32 s68, 0, 0x14000
	v_add_u32_e32 v202, s2, v189
	v_add_u32_e32 v203, s2, v190
	s_add_i32 s2, 0, 0x1c800
	v_mov_b32_e32 v155, v159
	v_mov_b32_e32 v157, v159
	v_bfe_u32 v188, v1, 4, 2
	v_mov_b32_e32 v161, v159
	v_lshl_add_u32 v162, v3, 1, v4
	v_mov_b32_e32 v163, v159
	v_mov_b64_e32 v[164:165], 0x100
	v_mov_b64_e32 v[166:167], 0xff
	v_add_u32_e32 v191, s67, v189
	v_add_u32_e32 v192, s67, v190
	v_add_u32_e32 v195, s68, v189
	v_add_u32_e32 v196, s68, v190
	v_add_u32_e32 v200, 0, v5
	v_add_u32_e32 v201, 0, v2
	v_add_u32_e32 v204, s2, v189
	v_add_u32_e32 v205, s2, v190
	s_movk_i32 s69, 0x7fff
	s_add_i32 s70, 0, 0x4300
	s_movk_i32 s71, 0x140
	s_add_i32 s76, 0, 0x19700
	v_mov_b32_e32 v206, 0x358637bd
	s_mov_b32 s77, 0x3fb8aa3b
	s_mov_b32 s78, 0xc2ce8ed0
	s_mov_b32 s79, 0x42b17218
	v_mov_b32_e32 v207, 0x7f800000
	v_mov_b32_e32 v208, 0x7fc00000
	s_mov_b32 s92, 0
	s_barrier
	s_branch .LBB0_1927

; __device__ __forceinline__ int tidx() { int t = threadIdx.x; asm volatile("" : "+v"(t)); return t; }
; __host__ __device__ __forceinline__ int lds_byte(int r, int c) { return (r >> 3) * 1024 + (r & 7) * 128 + ((((c >> 3) ^ r) & 7) << 4) + (c & 7) * 2; }
; #define PG8_STAGE(bufoff, gbase, voff) do { _Pragma("unroll") for (int _i = 0; _i < 2; ++_i) \
;         __builtin_amdgcn_global_load_lds((const unsigned*)((const char*)(gbase) + (voff)[_i]), (LAS unsigned*)(lds + (bufoff) + ldsw + _i * 8192), 16, 0, 0); } while (0)
; #define PG8_WAIT_V(n) asm volatile("s_waitcnt vmcnt(" #n ")" ::: "memory")
; #define PG8_BAR __builtin_amdgcn_s_barrier()
;     const int tid = tidx(), wid = __builtin_amdgcn_readfirstlane(tid >> 6), lane = tid & 63, wr = wid >> 2, wc = wid & 3, fr = lane & 15, fq = lane >> 4;
;     const int K = (int)g.K, ntf = K / BK;
;     int sR[2], sC[2]; unsigned voffB[2], voffA[2][2], voffN[2][2];
; #pragma unroll
;     for (int i = 0; i < 2; ++i) { stage_rc(tid * 16 + i * 8192, sR[i], sC[i]); const int Rb = Epi::PERM ? ((sR[i] & ~31) + perm32(sR[i] & 31)) : sR[i];
;         voffB[i] = (TILED & 2) ? (unsigned)(Rb * BK + sC[i]) * 2u : (unsigned)(Rb * K + sC[i]) * 2u; }
;     constexpr size_t kstepA = (TILED & 1) ? (size_t)HALF * BK * 2 : (size_t)(BK * 2), kstepB = (TILED & 2) ? (size_t)HALF * BK * 2 : (size_t)(BK * 2);
;     const size_t hstep = (size_t)HALF * K * 2;
;     const size_t tstep = 2 * hstep;
;     const unsigned ldsw = (unsigned)wid * 1024u;
;     const int aoff = lds_byte(wr * 64 + fr, fq * 8), boff = lds_byte(wc * 32 + fr, fq * 8);
;     ...
;     const char* cA = (const char*)(g.A + (size_t)cur.z * g.aStrideZ) + (GATHER ? (size_t)0 : (size_t)cur.pm * tstep) + k0t(cur) * kstepA;
;     const char* cB = (const char*)(g.Bt + (size_t)cur.z * g.bStrideZ) + (size_t)cur.pn * tstep + k0t(cur) * kstepB;
;     PG8_STAGE(PG8_SB(0, 0), cB, voffB); PG8_STAGE(PG8_SB(0, 1), cB + hstep, voffB); PG8_STAGE(PG8_SA(0, 0), cA, voffA[0]); PG8_STAGE(PG8_SA(0, 1), cA, voffA[1]);
;     if (wr == 1) PG8_BAR;
;     PG8_WAIT_V(2); PG8_BAR;
;     PG8_STAGE(PG8_SB(1, 0), cB + kstepB, voffB); PG8_STAGE(PG8_SA(1, 0), cA + kstepA, voffA[0]); PG8_STAGE(PG8_SB(1, 1), cB + hstep + kstepB, voffB);
;     PG8_WAIT_V(6); PG8_BAR;
.LBB0_2329:
	s_lshl_b32 s7, s7, 3
	s_lshl_b32 s39, s6, 6
	s_lshl_b32 s6, s0, 5
	s_sub_i32 s1, s1, s7
	s_and_b32 s40, s6, 0x60
	s_add_u32 s6, s2, 0x4000
	s_addc_u32 s7, s3, 0
	s_add_i32 m0, s17, 0x18000
	v_lshl_add_u64 v[4:5], s[6:7], 0, v[132:133]
	global_load_lds_dwordx4 v[4:5], off
	s_add_i32 m0, s17, 0x1a000
	v_lshl_add_u64 v[4:5], s[6:7], 0, v[134:135]
	s_add_u32 s6, s90, 0x4213680
	s_addc_u32 s7, s91, 0
	s_add_i32 s41, s17, 0x8000
	s_add_i32 s42, s17, 0xa000
	global_load_lds_dwordx4 v[4:5], off
	v_lshl_add_u64 v[4:5], s[6:7], 0, v[136:137]
	s_mov_b32 m0, s41
	s_add_u32 s10, s2, 0x44000
	global_load_lds_dwordx4 v[4:5], off
	v_lshl_add_u64 v[2:3], s[6:7], 0, v[2:3]
	s_mov_b32 m0, s42
	s_addc_u32 s11, s3, 0
	global_load_lds_dwordx4 v[2:3], off
	s_add_i32 m0, s17, 0x1c000
	v_lshl_add_u64 v[2:3], s[10:11], 0, v[132:133]
	global_load_lds_dwordx4 v[2:3], off
	v_lshl_add_u64 v[2:3], s[10:11], 0, v[134:135]
	s_add_i32 m0, s17, 0x1e000
	v_bfe_u32 v4, v6, 4, 2
	global_load_lds_dwordx4 v[2:3], off
	s_waitcnt vmcnt(8)
	s_barrier
	v_lshrrev_b32_e32 v2, 4, v6
	v_and_b32_e32 v3, 15, v6
	v_and_b32_e32 v6, 7, v6
	v_bitop3_b32 v2, v2, v6, 3 bitop3:0x6c
	s_cmpk_lt_u32 s8, 0x100
	v_lshlrev_b32_e32 v7, 4, v2
	v_or_b32_e32 v2, s40, v3
	s_cselect_b64 s[8:9], -1, 0
	s_lshl_b32 s0, s0, 6
	v_or_b32_e32 v5, s39, v3
	v_lshlrev_b32_e32 v9, 7, v2
	v_and_or_b32 v2, s39, 64, v3
	s_and_b32 s0, s0, 64
	s_sext_i32_i8 s52, s1
	v_lshlrev_b32_e32 v5, 7, v5
	s_waitcnt vmcnt(6)
	v_lshl_or_b32 v136, v4, 4, s0
	v_readlane_b32 s0, v250, 32
	v_lshlrev_b32_e32 v2, 6, v2
	v_or_b32_e32 v8, v5, v7
	v_readlane_b32 s1, v250, 33
	v_or_b32_e32 v4, 0x800, v2
	v_or_b32_e32 v6, 0xc00, v2
	v_bitop3_b32 v3, v5, 64, v7 bitop3:0x36
	v_or_b32_e32 v159, v9, v7
	v_lshl_add_u64 v[138:139], s[0:1], 0, v[136:137]
	v_bitop3_b32 v160, v9, 64, v7 bitop3:0x36
	s_add_i32 s43, 0, 0x10000
	s_add_i32 s44, 0, 0x10800
	s_add_i32 s45, 0, 0x14000
	s_add_i32 s46, 0, 0x14800
	v_add_u32_e32 v161, 0, v8
	v_add_u32_e32 v162, 0, v3
	s_add_i32 s47, 0, 0x18800
	s_add_i32 s48, 0, 0x1c800
	s_mov_b64 s[10:11], 0x80
	v_lshlrev_b32_e32 v140, 1, v2
	v_lshlrev_b32_e32 v142, 1, v4
	v_lshlrev_b32_e32 v144, 1, v6
	v_mov_b32_e32 v163, 0xc60000
	s_barrier
	s_branch .LBB0_2332

; __device__ __forceinline__ int tidx() { int t = threadIdx.x; asm volatile("" : "+v"(t)); return t; }
; __host__ __device__ __forceinline__ int lds_byte(int r, int c) { return (r >> 3) * 1024 + (r & 7) * 128 + ((((c >> 3) ^ r) & 7) << 4) + (c & 7) * 2; }
; #define PG8_STAGE(bufoff, gbase, voff) do { _Pragma("unroll") for (int _i = 0; _i < 2; ++_i) \
;         __builtin_amdgcn_global_load_lds((const unsigned*)((const char*)(gbase) + (voff)[_i]), (LAS unsigned*)(lds + (bufoff) + ldsw + _i * 8192), 16, 0, 0); } while (0)
; #define PG8_WAIT_V(n) asm volatile("s_waitcnt vmcnt(" #n ")" ::: "memory")
; #define PG8_BAR __builtin_amdgcn_s_barrier()
;     const int tid = tidx(), wid = __builtin_amdgcn_readfirstlane(tid >> 6), lane = tid & 63, wr = wid >> 2, wc = wid & 3, fr = lane & 15, fq = lane >> 4;
;     const int K = (int)g.K, ntf = K / BK;
;     int sR[2], sC[2]; unsigned voffB[2], voffA[2][2], voffN[2][2];
; #pragma unroll
;     for (int i = 0; i < 2; ++i) { stage_rc(tid * 16 + i * 8192, sR[i], sC[i]); const int Rb = Epi::PERM ? ((sR[i] & ~31) + perm32(sR[i] & 31)) : sR[i];
;         voffB[i] = (TILED & 2) ? (unsigned)(Rb * BK + sC[i]) * 2u : (unsigned)(Rb * K + sC[i]) * 2u; }
;     constexpr size_t kstepA = (TILED & 1) ? (size_t)HALF * BK * 2 : (size_t)(BK * 2), kstepB = (TILED & 2) ? (size_t)HALF * BK * 2 : (size_t)(BK * 2);
;     const size_t hstep = (size_t)HALF * K * 2;
;     const size_t tstep = 2 * hstep;
;     const unsigned ldsw = (unsigned)wid * 1024u;
;     const int aoff = lds_byte(wr * 64 + fr, fq * 8), boff = lds_byte(wc * 32 + fr, fq * 8);
;     ...
;     const char* cA = (const char*)(g.A + (size_t)cur.z * g.aStrideZ) + (GATHER ? (size_t)0 : (size_t)cur.pm * tstep) + k0t(cur) * kstepA;
;     const char* cB = (const char*)(g.Bt + (size_t)cur.z * g.bStrideZ) + (size_t)cur.pn * tstep + k0t(cur) * kstepB;
;     PG8_STAGE(PG8_SB(0, 0), cB, voffB); PG8_STAGE(PG8_SB(0, 1), cB + hstep, voffB); PG8_STAGE(PG8_SA(0, 0), cA, voffA[0]); PG8_STAGE(PG8_SA(0, 1), cA, voffA[1]);
;     if (wr == 1) PG8_BAR;
;     PG8_WAIT_V(2); PG8_BAR;
;     PG8_STAGE(PG8_SB(1, 0), cB + kstepB, voffB); PG8_STAGE(PG8_SA(1, 0), cA + kstepA, voffA[0]); PG8_STAGE(PG8_SB(1, 1), cB + hstep + kstepB, voffB);
;     PG8_WAIT_V(6); PG8_BAR;
.LBB0_2401:
	s_lshl_b32 s5, s5, 5
	s_and_b32 s7, s5, 0x60
	s_add_u32 s8, s20, 0x4000
	s_addc_u32 s9, s21, 0
	s_add_i32 m0, s34, 0x18000
	v_lshl_add_u64 v[10:11], s[8:9], 0, v[132:133]
	global_load_lds_dwordx4 v[10:11], off
	s_add_i32 m0, s34, 0x1a000
	v_lshl_add_u64 v[10:11], s[8:9], 0, v[130:131]
	s_add_u32 s8, s18, 0x4000
	s_addc_u32 s9, s19, 0
	s_add_i32 s39, s34, 0x8000
	global_load_lds_dwordx4 v[10:11], off
	v_lshl_add_u64 v[10:11], s[8:9], 0, v[134:135]
	s_mov_b32 m0, s39
	s_add_i32 s40, s34, 0xa000
	global_load_lds_dwordx4 v[10:11], off
	v_lshl_add_u64 v[10:11], s[8:9], 0, v[136:137]
	s_add_u32 s8, s20, 0xb4000
	s_mov_b32 m0, s40
	s_addc_u32 s9, s21, 0
	global_load_lds_dwordx4 v[10:11], off
	s_add_i32 m0, s34, 0x1c000
	v_lshl_add_u64 v[10:11], s[8:9], 0, v[132:133]
	global_load_lds_dwordx4 v[10:11], off
	v_lshl_add_u64 v[10:11], s[8:9], 0, v[130:131]
	s_add_i32 m0, s34, 0x1e000
	v_lshrrev_b32_e32 v9, 4, v3
	global_load_lds_dwordx4 v[10:11], off
	s_waitcnt vmcnt(8)
	s_barrier
	v_and_b32_e32 v10, 15, v3
	v_bfe_u32 v11, v3, 4, 2
	v_and_b32_e32 v3, 7, v3
	v_lshl_or_b32 v1, s4, 6, v10
	v_bitop3_b32 v3, v9, v3, 3 bitop3:0x6c
	v_or_b32_e32 v10, s7, v10
	v_lshlrev_b32_e32 v3, 4, v3
	v_lshlrev_b32_e32 v10, 7, v10
	s_cmpk_lt_u32 s1, 0x100
	s_sext_i32_i8 s53, s0
	v_or_b32_e32 v150, v10, v3
	s_cselect_b64 s[4:5], -1, 0
	v_bitop3_b32 v151, v10, 64, v3 bitop3:0x36
	s_add_i32 s0, 0, 0x10800
	v_lshlrev_b32_e32 v6, 7, v6
	v_lshlrev_b32_e32 v4, 7, v4
	v_add_u32_e32 v155, s0, v150
	v_add_u32_e32 v156, s0, v151
	s_add_i32 s0, 0, 0x14800
	v_lshlrev_b32_e32 v12, 7, v1
	s_waitcnt vmcnt(6)
	v_lshl_add_u32 v6, v7, 10, v6
	v_lshl_add_u32 v2, v2, 10, v4
	v_add_u32_e32 v159, s0, v150
	v_add_u32_e32 v160, s0, v151
	s_add_i32 s0, 0, 0x18800
	v_or_b32_e32 v9, v12, v3
	v_bitop3_b32 v3, v12, 64, v3 bitop3:0x36
	v_or_b32_e32 v6, v6, v8
	v_or_b32_e32 v2, v2, v5
	s_add_i32 s42, 0, 0x10000
	s_add_i32 s43, 0, 0x14000
	v_add_u32_e32 v163, s0, v150
	v_add_u32_e32 v164, s0, v151
	s_add_i32 s0, 0, 0x1c800
	v_mov_b32_e32 v139, v133
	v_mov_b32_e32 v141, v133
	s_sext_i32_i8 s52, s6
	s_ashr_i32 s41, s33, 3
	v_lshl_or_b32 v152, v11, 3, s7
	v_add_u32_e32 v142, 0xb0000, v6
	v_mov_b32_e32 v143, v133
	v_add_u32_e32 v144, 0xb0000, v2
	v_mov_b32_e32 v145, v133
	v_add_u32_e32 v153, s42, v150
	v_add_u32_e32 v154, s42, v151
	v_add_u32_e32 v157, s43, v150
	v_add_u32_e32 v158, s43, v151
	v_add_u32_e32 v161, 0, v9
	v_add_u32_e32 v162, 0, v3
	v_add_u32_e32 v165, s0, v150
	v_add_u32_e32 v166, s0, v151
	s_mov_b64 s[6:7], 0x40000
	s_mov_b32 s44, 0x40000
	s_mov_b64 s[8:9], 0x48000
	s_mov_b32 s45, 0x48000
	s_mov_b64 s[10:11], 0x50000
	s_mov_b32 s46, 0x50000
	s_mov_b64 s[12:13], 0x58000
	s_mov_b32 s47, 0x58000
	s_barrier
	s_branch .LBB0_2404
